# pre-converter: no image-store drain before its final barrier (the grid barrier after in_proj covers it)
# speedup vs baseline: 1.0042x; 1.0042x over previous
; __device__ __forceinline__ int lane_id() { int r; asm volatile("v_mbcnt_lo_u32_b32 %0, -1, 0\n\tv_mbcnt_hi_u32_b32 %0, -1, %0" : "=v"(r)); return r; }
; template <int LDB>
; __device__ __forceinline__ void convert_image(const float* __restrict__ W, int col0, int col1, unsigned char* __restrict__ img, LAS3 char* lds, int wid) {
;     int lane = lane_id(); asm volatile("" : "+v"(lane));
;     const int n4 = lane, half = n4 >> 5, nloc = (n4 & 31) * 4;
;     const float* src = W + (size_t)(wid * 16) * LDB + ((n4 < 32) ? col0 + n4 * 4 : col1 + (n4 - 32) * 4);
;     const unsigned cpo = (unsigned)(wid * 4096 + lane * 16);
; template <int EPI>
; __device__ __forceinline__ int* moe_phase(const Params& p, LAS3 char* lds, int wid, int* pend_in) {
;     ...
;                 const int e = qq + 8 * (sl / NCOL), pn = sl % NCOL;
;                 const int ecnt = __builtin_amdgcn_readfirstlane(xcnt[e]), ebase = __builtin_amdgcn_readfirstlane(xcnt[32 + e]), abase = __builtin_amdgcn_readfirstlane(xcnt[64 + e]); g.abase = abase;
;                 if (k < ((ecnt + 255) >> 8)) {
;                     TileSync sy{}; sy.flag = p.flag + ((EPI == 2) ? 0 : NE * 16) + e * NCOL + pn; sy.qctr = qctr + qq; sy.qtag = (unsigned)qq << 20; sy.qslot = slot + (par ^ 1);
;                     if (MOE_MERGED) { sy.pend = pend; if (EPI == 3) { sy.dep = p.done + e * 32 + k; sy.depn = 16; } }
;                     unsigned char* img = ((EPI == 2) ? p.img_gu : p.img_dn) + (size_t)(e * NCOL + pn) * 524288;
.LBB0_75:
	s_cmpk_lg_i32 s80, 0x100
	s_cbranch_scc1 .Lpc_skip
	s_lshr_b32 s1, s35, 3
	s_lshr_b32 s4, s35, 5
	s_add_u32 s1, s1, s4
	s_and_b32 s1, s1, 3
	s_lshr_b32 s0, s87, 8
	s_cmp_lg_u32 s0, s1
	s_cbranch_scc1 .Lpc_skip
	v_readlane_b32 s0, v254, 18
	v_readlane_b32 s1, v254, 19
	s_lshr_b32 s100, s35, 5
	s_and_b32 s101, s35, 31
	s_sub_u32 s88, s101, 16
	s_lshr_b32 s4, s88, 3
	s_lshl_b32 s4, s4, 3
	s_add_u32 s4, s4, s100
	s_and_b32 s5, s88, 7
	s_cmp_lt_u32 s101, 16
	s_cselect_b32 vcc_lo, 1, 0
	s_cselect_b32 s4, s100, s4
	s_cselect_b32 s5, s101, s5
	s_sub_u32 s0, s0, 0x140
	s_subb_u32 s1, s1, 0
	s_lshl_b32 s6, vcc_lo, 4
	s_sub_u32 s6, 0x80, s6
	s_lshl_b32 s88, vcc_lo, 3
	s_sub_u32 s88, 0x120, s88
	s_load_dwordx2 s[100:101], s[0:1], s6
	s_load_dwordx2 s[6:7], s[0:1], s88
	s_load_dwordx2 s[0:1], s[0:1], 0x128
	s_waitcnt lgkmcnt(0)
	s_add_u32 s88, vcc_lo, 24
	s_lshl_b32 s88, s4, s88
	s_add_u32 s100, s100, s88
	s_addc_u32 s101, s101, 0
	s_sub_u32 s88, 10, vcc_lo
	s_lshl_b32 s88, s5, s88
	s_add_u32 s100, s100, s88
	s_addc_u32 s101, s101, 0
	s_lshr_b32 vcc_hi, s75, 6
	s_add_u32 s88, vcc_lo, 17
	s_lshl_b32 s88, vcc_hi, s88
	s_add_u32 s100, s100, s88
	s_addc_u32 s101, s101, 0
	s_add_u32 s88, vcc_lo, 3
	s_lshl_b32 s88, s4, s88
	s_add_u32 s88, s88, s5
	s_lshl_b32 s4, s88, 19
	s_add_u32 s6, s6, s4
	s_addc_u32 s7, s7, 0
	s_xor_b32 s4, vcc_lo, 1
	s_lshl_b32 s4, s4, 9
	s_add_u32 s4, s4, s88
	s_lshl_b32 s4, s4, 2
	s_add_u32 s0, s0, s4
	s_addc_u32 s1, s1, 0
	v_mbcnt_lo_u32_b32 v131, -1, 0
	v_mbcnt_hi_u32_b32 v131, -1, v131
	s_add_u32 s4, vcc_lo, 13
	s_lshl_b32 s5, 1, s4
	s_lshl_b32 s88, vcc_lo, 2
	s_add_u32 s88, s88, 9
	s_lshl_b32 s88, 1, s88
	v_and_b32_e32 v132, 31, v131
	v_lshrrev_b32_e32 v150, 5, v131
	v_lshlrev_b32_e32 v132, 4, v132
	v_mad_u32_u24 v132, v150, s88, v132
	v_add_u32_e32 v133, s5, v132
	v_add_u32_e32 v134, s5, v133
	v_add_u32_e32 v135, s5, v134
	v_add_u32_e32 v136, s5, v135
	v_add_u32_e32 v137, s5, v136
	v_add_u32_e32 v138, s5, v137
	v_add_u32_e32 v139, s5, v138
	v_add_u32_e32 v140, s5, v139
	v_add_u32_e32 v141, s5, v140
	v_add_u32_e32 v142, s5, v141
	v_add_u32_e32 v143, s5, v142
	v_add_u32_e32 v144, s5, v143
	v_add_u32_e32 v145, s5, v144
	v_add_u32_e32 v146, s5, v145
	v_add_u32_e32 v147, s5, v146
	v_and_b32_e32 v151, 3, v131
	v_lshlrev_b32_e32 v151, 1, v151
	v_xor_b32_e32 v148, vcc_hi, v151
	v_or_b32_e32 v151, 1, v151
	v_xor_b32_e32 v149, vcc_hi, v151
	v_lshlrev_b32_e32 v148, 4, v148
	v_lshlrev_b32_e32 v149, 4, v149
	v_and_b32_e32 v151, 31, v131
	v_lshlrev_b32_e32 v151, 9, v151
	v_lshl_add_u32 v151, v150, 14, v151
	v_add_u32_e32 v148, v148, v151
	v_add_u32_e32 v149, v149, v151
	v_add_u32_e32 v149, 0x100, v149
	v_lshlrev_b32_e32 v150, 4, v131
	s_lshl_b32 s4, vcc_hi, 12
	v_add_u32_e32 v150, s4, v150
	s_lshl_b32 s88, s5, 7
	s_mov_b32 s5, 0x3b800000
	global_load_dwordx4 v[0:3], v132, s[100:101] nt
	global_load_dwordx4 v[4:7], v133, s[100:101] nt
	global_load_dwordx4 v[8:11], v134, s[100:101] nt
	global_load_dwordx4 v[12:15], v135, s[100:101] nt
	global_load_dwordx4 v[16:19], v136, s[100:101] nt
	global_load_dwordx4 v[20:23], v137, s[100:101] nt
	global_load_dwordx4 v[24:27], v138, s[100:101] nt
	global_load_dwordx4 v[28:31], v139, s[100:101] nt
	global_load_dwordx4 v[32:35], v140, s[100:101] nt
	global_load_dwordx4 v[36:39], v141, s[100:101] nt
	global_load_dwordx4 v[40:43], v142, s[100:101] nt
	global_load_dwordx4 v[44:47], v143, s[100:101] nt
	global_load_dwordx4 v[48:51], v144, s[100:101] nt
	global_load_dwordx4 v[52:55], v145, s[100:101] nt
	global_load_dwordx4 v[56:59], v146, s[100:101] nt
	global_load_dwordx4 v[60:63], v147, s[100:101] nt
	s_add_u32 s100, s100, s88
	s_addc_u32 s101, s101, 0
	global_load_dwordx4 v[64:67], v132, s[100:101] nt
	global_load_dwordx4 v[68:71], v133, s[100:101] nt
	global_load_dwordx4 v[72:75], v134, s[100:101] nt
	global_load_dwordx4 v[76:79], v135, s[100:101] nt
	global_load_dwordx4 v[80:83], v136, s[100:101] nt
	global_load_dwordx4 v[84:87], v137, s[100:101] nt
	global_load_dwordx4 v[88:91], v138, s[100:101] nt
	global_load_dwordx4 v[92:95], v139, s[100:101] nt
	global_load_dwordx4 v[96:99], v140, s[100:101] nt
	global_load_dwordx4 v[100:103], v141, s[100:101] nt
	global_load_dwordx4 v[104:107], v142, s[100:101] nt
	global_load_dwordx4 v[108:111], v143, s[100:101] nt
	global_load_dwordx4 v[112:115], v144, s[100:101] nt
	global_load_dwordx4 v[116:119], v145, s[100:101] nt
	global_load_dwordx4 v[120:123], v146, s[100:101] nt
	global_load_dwordx4 v[124:127], v147, s[100:101] nt
	s_add_u32 s100, s100, s88
	s_addc_u32 s101, s101, 0
	global_load_dwordx4 v[184:187], v132, s[100:101] nt
	global_load_dwordx4 v[188:191], v133, s[100:101] nt
	global_load_dwordx4 v[192:195], v134, s[100:101] nt
	global_load_dwordx4 v[196:199], v135, s[100:101] nt
	global_load_dwordx4 v[200:203], v136, s[100:101] nt
	global_load_dwordx4 v[204:207], v137, s[100:101] nt
	global_load_dwordx4 v[208:211], v138, s[100:101] nt
	global_load_dwordx4 v[212:215], v139, s[100:101] nt
	global_load_dwordx4 v[216:219], v140, s[100:101] nt
	global_load_dwordx4 v[220:223], v141, s[100:101] nt
	global_load_dwordx4 v[224:227], v142, s[100:101] nt
	global_load_dwordx4 v[228:231], v143, s[100:101] nt
	global_load_dwordx4 v[232:235], v144, s[100:101] nt
	global_load_dwordx4 v[236:239], v145, s[100:101] nt
	global_load_dwordx4 v[240:243], v146, s[100:101] nt
	global_load_dwordx4 v[244:247], v147, s[100:101] nt
	s_waitcnt vmcnt(32)
; #define G_SCHED __builtin_amdgcn_sched_barrier(0)
; #define CI_LOAD(R, kt) do { _Pragma("unroll") for (int _j = 0; _j < 16; ++_j) R[_j] = __builtin_nontemporal_load((const f32x4*)(src + (size_t)((kt) * 128 + _j) * LDB)); } while (0)
; template <int LDB>
; __device__ __forceinline__ void convert_image(const float* __restrict__ W, int col0, int col1, unsigned char* __restrict__ img, LAS3 char* lds, int wid) {
;     ...
;     f32x4 ra[16], rb[16];
;     CI_LOAD(ra, 0);
;     for (int kt = 0; kt < 16; kt += 2) {
;         CI_LOAD(rb, kt + 1); G_SCHED;
;         CI_CONV(ra, kt); G_SCHED;
;         CI_LOAD(ra, (kt + 2 < 16) ? kt + 2 : 15); G_SCHED;
	v_cvt_scalef32_pk_fp8_f32 v152, v0, v4, s5
	v_cvt_scalef32_pk_fp8_f32 v156, v1, v5, s5
	v_cvt_scalef32_pk_fp8_f32 v160, v2, v6, s5
	v_cvt_scalef32_pk_fp8_f32 v164, v3, v7, s5
	v_cvt_scalef32_pk_fp8_f32 v153, v16, v20, s5
	v_cvt_scalef32_pk_fp8_f32 v157, v17, v21, s5
	v_cvt_scalef32_pk_fp8_f32 v161, v18, v22, s5
	v_cvt_scalef32_pk_fp8_f32 v165, v19, v23, s5
	v_cvt_scalef32_pk_fp8_f32 v154, v32, v36, s5
	v_cvt_scalef32_pk_fp8_f32 v158, v33, v37, s5
	v_cvt_scalef32_pk_fp8_f32 v162, v34, v38, s5
	v_cvt_scalef32_pk_fp8_f32 v166, v35, v39, s5
	v_cvt_scalef32_pk_fp8_f32 v155, v48, v52, s5
	v_cvt_scalef32_pk_fp8_f32 v159, v49, v53, s5
	v_cvt_scalef32_pk_fp8_f32 v163, v50, v54, s5
	v_cvt_scalef32_pk_fp8_f32 v167, v51, v55, s5
	v_cvt_scalef32_pk_fp8_f32 v152, v8, v12, s5 op_sel:[0,0,0,1]
	v_cvt_scalef32_pk_fp8_f32 v156, v9, v13, s5 op_sel:[0,0,0,1]
	v_cvt_scalef32_pk_fp8_f32 v160, v10, v14, s5 op_sel:[0,0,0,1]
	v_cvt_scalef32_pk_fp8_f32 v164, v11, v15, s5 op_sel:[0,0,0,1]
	v_cvt_scalef32_pk_fp8_f32 v153, v24, v28, s5 op_sel:[0,0,0,1]
	v_cvt_scalef32_pk_fp8_f32 v157, v25, v29, s5 op_sel:[0,0,0,1]
	v_cvt_scalef32_pk_fp8_f32 v161, v26, v30, s5 op_sel:[0,0,0,1]
	v_cvt_scalef32_pk_fp8_f32 v165, v27, v31, s5 op_sel:[0,0,0,1]
	v_cvt_scalef32_pk_fp8_f32 v154, v40, v44, s5 op_sel:[0,0,0,1]
	v_cvt_scalef32_pk_fp8_f32 v158, v41, v45, s5 op_sel:[0,0,0,1]
	v_cvt_scalef32_pk_fp8_f32 v162, v42, v46, s5 op_sel:[0,0,0,1]
	v_cvt_scalef32_pk_fp8_f32 v166, v43, v47, s5 op_sel:[0,0,0,1]
	v_cvt_scalef32_pk_fp8_f32 v155, v56, v60, s5 op_sel:[0,0,0,1]
	v_cvt_scalef32_pk_fp8_f32 v159, v57, v61, s5 op_sel:[0,0,0,1]
	v_cvt_scalef32_pk_fp8_f32 v163, v58, v62, s5 op_sel:[0,0,0,1]
	v_cvt_scalef32_pk_fp8_f32 v167, v59, v63, s5 op_sel:[0,0,0,1]
	s_add_u32 s100, s100, s88
	s_addc_u32 s101, s101, 0
	global_load_dwordx4 v[0:3], v132, s[100:101] nt
	global_load_dwordx4 v[4:7], v133, s[100:101] nt
	global_load_dwordx4 v[8:11], v134, s[100:101] nt
	global_load_dwordx4 v[12:15], v135, s[100:101] nt
	global_load_dwordx4 v[16:19], v136, s[100:101] nt
	global_load_dwordx4 v[20:23], v137, s[100:101] nt
	global_load_dwordx4 v[24:27], v138, s[100:101] nt
	global_load_dwordx4 v[28:31], v139, s[100:101] nt
	global_load_dwordx4 v[32:35], v140, s[100:101] nt
	global_load_dwordx4 v[36:39], v141, s[100:101] nt
	global_load_dwordx4 v[40:43], v142, s[100:101] nt
	global_load_dwordx4 v[44:47], v143, s[100:101] nt
	global_load_dwordx4 v[48:51], v144, s[100:101] nt
	global_load_dwordx4 v[52:55], v145, s[100:101] nt
	global_load_dwordx4 v[56:59], v146, s[100:101] nt
	global_load_dwordx4 v[60:63], v147, s[100:101] nt
	ds_write_b128 v148, v[152:155] offset:0
	ds_write_b128 v148, v[156:159] offset:128
	ds_write_b128 v149, v[160:163] offset:0
	ds_write_b128 v149, v[164:167] offset:128
	s_waitcnt lgkmcnt(0)
	s_barrier
	ds_read_b128 v[168:171], v150 offset:0
	ds_read_b128 v[172:175], v150 offset:1024
	ds_read_b128 v[176:179], v150 offset:2048
	ds_read_b128 v[180:183], v150 offset:3072
	s_waitcnt lgkmcnt(3)
	global_store_dwordx4 v150, v[168:171], s[6:7] nt
	s_waitcnt lgkmcnt(2)
	global_store_dwordx4 v150, v[172:175], s[6:7] offset:1024 nt
	s_waitcnt lgkmcnt(1)
	global_store_dwordx4 v150, v[176:179], s[6:7] offset:2048 nt
	s_waitcnt lgkmcnt(0)
	global_store_dwordx4 v150, v[180:183], s[6:7] offset:3072 nt
	s_add_u32 s6, s6, 0x8000
	s_addc_u32 s7, s7, 0
	s_waitcnt vmcnt(36)
	v_cvt_scalef32_pk_fp8_f32 v152, v64, v68, s5
	v_cvt_scalef32_pk_fp8_f32 v156, v65, v69, s5
	v_cvt_scalef32_pk_fp8_f32 v160, v66, v70, s5
	v_cvt_scalef32_pk_fp8_f32 v164, v67, v71, s5
	v_cvt_scalef32_pk_fp8_f32 v153, v80, v84, s5
	v_cvt_scalef32_pk_fp8_f32 v157, v81, v85, s5
	v_cvt_scalef32_pk_fp8_f32 v161, v82, v86, s5
	v_cvt_scalef32_pk_fp8_f32 v165, v83, v87, s5
	v_cvt_scalef32_pk_fp8_f32 v154, v96, v100, s5
	v_cvt_scalef32_pk_fp8_f32 v158, v97, v101, s5
	v_cvt_scalef32_pk_fp8_f32 v162, v98, v102, s5
	v_cvt_scalef32_pk_fp8_f32 v166, v99, v103, s5
	v_cvt_scalef32_pk_fp8_f32 v155, v112, v116, s5
	v_cvt_scalef32_pk_fp8_f32 v159, v113, v117, s5
	v_cvt_scalef32_pk_fp8_f32 v163, v114, v118, s5
	v_cvt_scalef32_pk_fp8_f32 v167, v115, v119, s5
	v_cvt_scalef32_pk_fp8_f32 v152, v72, v76, s5 op_sel:[0,0,0,1]
	v_cvt_scalef32_pk_fp8_f32 v156, v73, v77, s5 op_sel:[0,0,0,1]
	v_cvt_scalef32_pk_fp8_f32 v160, v74, v78, s5 op_sel:[0,0,0,1]
	v_cvt_scalef32_pk_fp8_f32 v164, v75, v79, s5 op_sel:[0,0,0,1]
	v_cvt_scalef32_pk_fp8_f32 v153, v88, v92, s5 op_sel:[0,0,0,1]
	v_cvt_scalef32_pk_fp8_f32 v157, v89, v93, s5 op_sel:[0,0,0,1]
	v_cvt_scalef32_pk_fp8_f32 v161, v90, v94, s5 op_sel:[0,0,0,1]
	v_cvt_scalef32_pk_fp8_f32 v165, v91, v95, s5 op_sel:[0,0,0,1]
	v_cvt_scalef32_pk_fp8_f32 v154, v104, v108, s5 op_sel:[0,0,0,1]
	v_cvt_scalef32_pk_fp8_f32 v158, v105, v109, s5 op_sel:[0,0,0,1]
	v_cvt_scalef32_pk_fp8_f32 v162, v106, v110, s5 op_sel:[0,0,0,1]
	v_cvt_scalef32_pk_fp8_f32 v166, v107, v111, s5 op_sel:[0,0,0,1]
	v_cvt_scalef32_pk_fp8_f32 v155, v120, v124, s5 op_sel:[0,0,0,1]
	v_cvt_scalef32_pk_fp8_f32 v159, v121, v125, s5 op_sel:[0,0,0,1]
	v_cvt_scalef32_pk_fp8_f32 v163, v122, v126, s5 op_sel:[0,0,0,1]
	v_cvt_scalef32_pk_fp8_f32 v167, v123, v127, s5 op_sel:[0,0,0,1]
	s_add_u32 s100, s100, s88
	s_addc_u32 s101, s101, 0
	global_load_dwordx4 v[64:67], v132, s[100:101] nt
	global_load_dwordx4 v[68:71], v133, s[100:101] nt
	global_load_dwordx4 v[72:75], v134, s[100:101] nt
	global_load_dwordx4 v[76:79], v135, s[100:101] nt
	global_load_dwordx4 v[80:83], v136, s[100:101] nt
	global_load_dwordx4 v[84:87], v137, s[100:101] nt
	global_load_dwordx4 v[88:91], v138, s[100:101] nt
	global_load_dwordx4 v[92:95], v139, s[100:101] nt
	global_load_dwordx4 v[96:99], v140, s[100:101] nt
	global_load_dwordx4 v[100:103], v141, s[100:101] nt
	global_load_dwordx4 v[104:107], v142, s[100:101] nt
	global_load_dwordx4 v[108:111], v143, s[100:101] nt
	global_load_dwordx4 v[112:115], v144, s[100:101] nt
	global_load_dwordx4 v[116:119], v145, s[100:101] nt
	global_load_dwordx4 v[120:123], v146, s[100:101] nt
	global_load_dwordx4 v[124:127], v147, s[100:101] nt
	ds_write_b128 v148, v[152:155] offset:32768
	ds_write_b128 v148, v[156:159] offset:32896
	ds_write_b128 v149, v[160:163] offset:32768
	ds_write_b128 v149, v[164:167] offset:32896
	s_waitcnt lgkmcnt(0)
	s_barrier
; #define G_SCHED __builtin_amdgcn_sched_barrier(0)
; #define CI_LOAD(R, kt) do { _Pragma("unroll") for (int _j = 0; _j < 16; ++_j) R[_j] = __builtin_nontemporal_load((const f32x4*)(src + (size_t)((kt) * 128 + _j) * LDB)); } while (0)
; template <int LDB>
; __device__ __forceinline__ void convert_image(const float* __restrict__ W, int col0, int col1, unsigned char* __restrict__ img, LAS3 char* lds, int wid) {
;     ...
;     f32x4 ra[16], rb[16];
;     CI_LOAD(ra, 0);
;     for (int kt = 0; kt < 16; kt += 2) {
;         CI_LOAD(rb, kt + 1); G_SCHED;
;         CI_CONV(ra, kt); G_SCHED;
;         CI_LOAD(ra, (kt + 2 < 16) ? kt + 2 : 15); G_SCHED;
	ds_read_b128 v[168:171], v150 offset:32768
	ds_read_b128 v[172:175], v150 offset:33792
	ds_read_b128 v[176:179], v150 offset:34816
	ds_read_b128 v[180:183], v150 offset:35840
	s_waitcnt lgkmcnt(3)
	global_store_dwordx4 v150, v[168:171], s[6:7] nt
	s_waitcnt lgkmcnt(2)
	global_store_dwordx4 v150, v[172:175], s[6:7] offset:1024 nt
	s_waitcnt lgkmcnt(1)
	global_store_dwordx4 v150, v[176:179], s[6:7] offset:2048 nt
	s_waitcnt lgkmcnt(0)
	global_store_dwordx4 v150, v[180:183], s[6:7] offset:3072 nt
	s_add_u32 s6, s6, 0x8000
	s_addc_u32 s7, s7, 0
	s_waitcnt vmcnt(40)
	v_cvt_scalef32_pk_fp8_f32 v152, v184, v188, s5
	v_cvt_scalef32_pk_fp8_f32 v156, v185, v189, s5
	v_cvt_scalef32_pk_fp8_f32 v160, v186, v190, s5
	v_cvt_scalef32_pk_fp8_f32 v164, v187, v191, s5
	v_cvt_scalef32_pk_fp8_f32 v153, v200, v204, s5
	v_cvt_scalef32_pk_fp8_f32 v157, v201, v205, s5
	v_cvt_scalef32_pk_fp8_f32 v161, v202, v206, s5
	v_cvt_scalef32_pk_fp8_f32 v165, v203, v207, s5
	v_cvt_scalef32_pk_fp8_f32 v154, v216, v220, s5
	v_cvt_scalef32_pk_fp8_f32 v158, v217, v221, s5
	v_cvt_scalef32_pk_fp8_f32 v162, v218, v222, s5
	v_cvt_scalef32_pk_fp8_f32 v166, v219, v223, s5
	v_cvt_scalef32_pk_fp8_f32 v155, v232, v236, s5
	v_cvt_scalef32_pk_fp8_f32 v159, v233, v237, s5
	v_cvt_scalef32_pk_fp8_f32 v163, v234, v238, s5
	v_cvt_scalef32_pk_fp8_f32 v167, v235, v239, s5
	v_cvt_scalef32_pk_fp8_f32 v152, v192, v196, s5 op_sel:[0,0,0,1]
	v_cvt_scalef32_pk_fp8_f32 v156, v193, v197, s5 op_sel:[0,0,0,1]
	v_cvt_scalef32_pk_fp8_f32 v160, v194, v198, s5 op_sel:[0,0,0,1]
	v_cvt_scalef32_pk_fp8_f32 v164, v195, v199, s5 op_sel:[0,0,0,1]
	v_cvt_scalef32_pk_fp8_f32 v153, v208, v212, s5 op_sel:[0,0,0,1]
	v_cvt_scalef32_pk_fp8_f32 v157, v209, v213, s5 op_sel:[0,0,0,1]
	v_cvt_scalef32_pk_fp8_f32 v161, v210, v214, s5 op_sel:[0,0,0,1]
	v_cvt_scalef32_pk_fp8_f32 v165, v211, v215, s5 op_sel:[0,0,0,1]
	v_cvt_scalef32_pk_fp8_f32 v154, v224, v228, s5 op_sel:[0,0,0,1]
	v_cvt_scalef32_pk_fp8_f32 v158, v225, v229, s5 op_sel:[0,0,0,1]
	v_cvt_scalef32_pk_fp8_f32 v162, v226, v230, s5 op_sel:[0,0,0,1]
	v_cvt_scalef32_pk_fp8_f32 v166, v227, v231, s5 op_sel:[0,0,0,1]
	v_cvt_scalef32_pk_fp8_f32 v155, v240, v244, s5 op_sel:[0,0,0,1]
	v_cvt_scalef32_pk_fp8_f32 v159, v241, v245, s5 op_sel:[0,0,0,1]
	v_cvt_scalef32_pk_fp8_f32 v163, v242, v246, s5 op_sel:[0,0,0,1]
	v_cvt_scalef32_pk_fp8_f32 v167, v243, v247, s5 op_sel:[0,0,0,1]
	s_add_u32 s100, s100, s88
	s_addc_u32 s101, s101, 0
	global_load_dwordx4 v[184:187], v132, s[100:101] nt
	global_load_dwordx4 v[188:191], v133, s[100:101] nt
	global_load_dwordx4 v[192:195], v134, s[100:101] nt
	global_load_dwordx4 v[196:199], v135, s[100:101] nt
	global_load_dwordx4 v[200:203], v136, s[100:101] nt
	global_load_dwordx4 v[204:207], v137, s[100:101] nt
	global_load_dwordx4 v[208:211], v138, s[100:101] nt
	global_load_dwordx4 v[212:215], v139, s[100:101] nt
	global_load_dwordx4 v[216:219], v140, s[100:101] nt
	global_load_dwordx4 v[220:223], v141, s[100:101] nt
	global_load_dwordx4 v[224:227], v142, s[100:101] nt
	global_load_dwordx4 v[228:231], v143, s[100:101] nt
	global_load_dwordx4 v[232:235], v144, s[100:101] nt
	global_load_dwordx4 v[236:239], v145, s[100:101] nt
	global_load_dwordx4 v[240:243], v146, s[100:101] nt
	global_load_dwordx4 v[244:247], v147, s[100:101] nt
	ds_write_b128 v148, v[152:155] offset:0
	ds_write_b128 v148, v[156:159] offset:128
	ds_write_b128 v149, v[160:163] offset:0
	ds_write_b128 v149, v[164:167] offset:128
	s_waitcnt lgkmcnt(0)
	s_barrier
	ds_read_b128 v[168:171], v150 offset:0
	ds_read_b128 v[172:175], v150 offset:1024
	ds_read_b128 v[176:179], v150 offset:2048
	ds_read_b128 v[180:183], v150 offset:3072
	s_waitcnt lgkmcnt(3)
	global_store_dwordx4 v150, v[168:171], s[6:7] nt
	s_waitcnt lgkmcnt(2)
	global_store_dwordx4 v150, v[172:175], s[6:7] offset:1024 nt
	s_waitcnt lgkmcnt(1)
	global_store_dwordx4 v150, v[176:179], s[6:7] offset:2048 nt
	s_waitcnt lgkmcnt(0)
	global_store_dwordx4 v150, v[180:183], s[6:7] offset:3072 nt
	s_add_u32 s6, s6, 0x8000
	s_addc_u32 s7, s7, 0
	s_waitcnt vmcnt(44)
	v_cvt_scalef32_pk_fp8_f32 v152, v0, v4, s5
	v_cvt_scalef32_pk_fp8_f32 v156, v1, v5, s5
	v_cvt_scalef32_pk_fp8_f32 v160, v2, v6, s5
	v_cvt_scalef32_pk_fp8_f32 v164, v3, v7, s5
	v_cvt_scalef32_pk_fp8_f32 v153, v16, v20, s5
	v_cvt_scalef32_pk_fp8_f32 v157, v17, v21, s5
	v_cvt_scalef32_pk_fp8_f32 v161, v18, v22, s5
	v_cvt_scalef32_pk_fp8_f32 v165, v19, v23, s5
	v_cvt_scalef32_pk_fp8_f32 v154, v32, v36, s5
	v_cvt_scalef32_pk_fp8_f32 v158, v33, v37, s5
	v_cvt_scalef32_pk_fp8_f32 v162, v34, v38, s5
	v_cvt_scalef32_pk_fp8_f32 v166, v35, v39, s5
	v_cvt_scalef32_pk_fp8_f32 v155, v48, v52, s5
	v_cvt_scalef32_pk_fp8_f32 v159, v49, v53, s5
	v_cvt_scalef32_pk_fp8_f32 v163, v50, v54, s5
	v_cvt_scalef32_pk_fp8_f32 v167, v51, v55, s5
	v_cvt_scalef32_pk_fp8_f32 v152, v8, v12, s5 op_sel:[0,0,0,1]
	v_cvt_scalef32_pk_fp8_f32 v156, v9, v13, s5 op_sel:[0,0,0,1]
	v_cvt_scalef32_pk_fp8_f32 v160, v10, v14, s5 op_sel:[0,0,0,1]
	v_cvt_scalef32_pk_fp8_f32 v164, v11, v15, s5 op_sel:[0,0,0,1]
	v_cvt_scalef32_pk_fp8_f32 v153, v24, v28, s5 op_sel:[0,0,0,1]
	v_cvt_scalef32_pk_fp8_f32 v157, v25, v29, s5 op_sel:[0,0,0,1]
	v_cvt_scalef32_pk_fp8_f32 v161, v26, v30, s5 op_sel:[0,0,0,1]
	v_cvt_scalef32_pk_fp8_f32 v165, v27, v31, s5 op_sel:[0,0,0,1]
	v_cvt_scalef32_pk_fp8_f32 v154, v40, v44, s5 op_sel:[0,0,0,1]
	v_cvt_scalef32_pk_fp8_f32 v158, v41, v45, s5 op_sel:[0,0,0,1]
	v_cvt_scalef32_pk_fp8_f32 v162, v42, v46, s5 op_sel:[0,0,0,1]
	v_cvt_scalef32_pk_fp8_f32 v166, v43, v47, s5 op_sel:[0,0,0,1]
	v_cvt_scalef32_pk_fp8_f32 v155, v56, v60, s5 op_sel:[0,0,0,1]
	v_cvt_scalef32_pk_fp8_f32 v159, v57, v61, s5 op_sel:[0,0,0,1]
	v_cvt_scalef32_pk_fp8_f32 v163, v58, v62, s5 op_sel:[0,0,0,1]
	v_cvt_scalef32_pk_fp8_f32 v167, v59, v63, s5 op_sel:[0,0,0,1]
	s_add_u32 s100, s100, s88
	s_addc_u32 s101, s101, 0
	global_load_dwordx4 v[0:3], v132, s[100:101] nt
	global_load_dwordx4 v[4:7], v133, s[100:101] nt
	global_load_dwordx4 v[8:11], v134, s[100:101] nt
	global_load_dwordx4 v[12:15], v135, s[100:101] nt
	global_load_dwordx4 v[16:19], v136, s[100:101] nt
	global_load_dwordx4 v[20:23], v137, s[100:101] nt
	global_load_dwordx4 v[24:27], v138, s[100:101] nt
	global_load_dwordx4 v[28:31], v139, s[100:101] nt
	global_load_dwordx4 v[32:35], v140, s[100:101] nt
	global_load_dwordx4 v[36:39], v141, s[100:101] nt
	global_load_dwordx4 v[40:43], v142, s[100:101] nt
	global_load_dwordx4 v[44:47], v143, s[100:101] nt
	global_load_dwordx4 v[48:51], v144, s[100:101] nt
	global_load_dwordx4 v[52:55], v145, s[100:101] nt
	global_load_dwordx4 v[56:59], v146, s[100:101] nt
	global_load_dwordx4 v[60:63], v147, s[100:101] nt
	ds_write_b128 v148, v[152:155] offset:32768
	ds_write_b128 v148, v[156:159] offset:32896
	ds_write_b128 v149, v[160:163] offset:32768
	ds_write_b128 v149, v[164:167] offset:32896
	s_waitcnt lgkmcnt(0)
	s_barrier
; #define G_SCHED __builtin_amdgcn_sched_barrier(0)
; #define CI_LOAD(R, kt) do { _Pragma("unroll") for (int _j = 0; _j < 16; ++_j) R[_j] = __builtin_nontemporal_load((const f32x4*)(src + (size_t)((kt) * 128 + _j) * LDB)); } while (0)
; template <int LDB>
; __device__ __forceinline__ void convert_image(const float* __restrict__ W, int col0, int col1, unsigned char* __restrict__ img, LAS3 char* lds, int wid) {
;     ...
;     f32x4 ra[16], rb[16];
;     CI_LOAD(ra, 0);
;     for (int kt = 0; kt < 16; kt += 2) {
;         CI_LOAD(rb, kt + 1); G_SCHED;
;         CI_CONV(ra, kt); G_SCHED;
;         CI_LOAD(ra, (kt + 2 < 16) ? kt + 2 : 15); G_SCHED;
	ds_read_b128 v[168:171], v150 offset:32768
	ds_read_b128 v[172:175], v150 offset:33792
	ds_read_b128 v[176:179], v150 offset:34816
	ds_read_b128 v[180:183], v150 offset:35840
	s_waitcnt lgkmcnt(3)
	global_store_dwordx4 v150, v[168:171], s[6:7] nt
	s_waitcnt lgkmcnt(2)
	global_store_dwordx4 v150, v[172:175], s[6:7] offset:1024 nt
	s_waitcnt lgkmcnt(1)
	global_store_dwordx4 v150, v[176:179], s[6:7] offset:2048 nt
	s_waitcnt lgkmcnt(0)
	global_store_dwordx4 v150, v[180:183], s[6:7] offset:3072 nt
	s_add_u32 s6, s6, 0x8000
	s_addc_u32 s7, s7, 0
	s_waitcnt vmcnt(44)
	v_cvt_scalef32_pk_fp8_f32 v152, v64, v68, s5
	v_cvt_scalef32_pk_fp8_f32 v156, v65, v69, s5
	v_cvt_scalef32_pk_fp8_f32 v160, v66, v70, s5
	v_cvt_scalef32_pk_fp8_f32 v164, v67, v71, s5
	v_cvt_scalef32_pk_fp8_f32 v153, v80, v84, s5
	v_cvt_scalef32_pk_fp8_f32 v157, v81, v85, s5
	v_cvt_scalef32_pk_fp8_f32 v161, v82, v86, s5
	v_cvt_scalef32_pk_fp8_f32 v165, v83, v87, s5
	v_cvt_scalef32_pk_fp8_f32 v154, v96, v100, s5
	v_cvt_scalef32_pk_fp8_f32 v158, v97, v101, s5
	v_cvt_scalef32_pk_fp8_f32 v162, v98, v102, s5
	v_cvt_scalef32_pk_fp8_f32 v166, v99, v103, s5
	v_cvt_scalef32_pk_fp8_f32 v155, v112, v116, s5
	v_cvt_scalef32_pk_fp8_f32 v159, v113, v117, s5
	v_cvt_scalef32_pk_fp8_f32 v163, v114, v118, s5
	v_cvt_scalef32_pk_fp8_f32 v167, v115, v119, s5
	v_cvt_scalef32_pk_fp8_f32 v152, v72, v76, s5 op_sel:[0,0,0,1]
	v_cvt_scalef32_pk_fp8_f32 v156, v73, v77, s5 op_sel:[0,0,0,1]
	v_cvt_scalef32_pk_fp8_f32 v160, v74, v78, s5 op_sel:[0,0,0,1]
	v_cvt_scalef32_pk_fp8_f32 v164, v75, v79, s5 op_sel:[0,0,0,1]
	v_cvt_scalef32_pk_fp8_f32 v153, v88, v92, s5 op_sel:[0,0,0,1]
	v_cvt_scalef32_pk_fp8_f32 v157, v89, v93, s5 op_sel:[0,0,0,1]
	v_cvt_scalef32_pk_fp8_f32 v161, v90, v94, s5 op_sel:[0,0,0,1]
	v_cvt_scalef32_pk_fp8_f32 v165, v91, v95, s5 op_sel:[0,0,0,1]
	v_cvt_scalef32_pk_fp8_f32 v154, v104, v108, s5 op_sel:[0,0,0,1]
	v_cvt_scalef32_pk_fp8_f32 v158, v105, v109, s5 op_sel:[0,0,0,1]
	v_cvt_scalef32_pk_fp8_f32 v162, v106, v110, s5 op_sel:[0,0,0,1]
	v_cvt_scalef32_pk_fp8_f32 v166, v107, v111, s5 op_sel:[0,0,0,1]
	v_cvt_scalef32_pk_fp8_f32 v155, v120, v124, s5 op_sel:[0,0,0,1]
	v_cvt_scalef32_pk_fp8_f32 v159, v121, v125, s5 op_sel:[0,0,0,1]
	v_cvt_scalef32_pk_fp8_f32 v163, v122, v126, s5 op_sel:[0,0,0,1]
	v_cvt_scalef32_pk_fp8_f32 v167, v123, v127, s5 op_sel:[0,0,0,1]
	s_add_u32 s100, s100, s88
	s_addc_u32 s101, s101, 0
	global_load_dwordx4 v[64:67], v132, s[100:101] nt
	global_load_dwordx4 v[68:71], v133, s[100:101] nt
	global_load_dwordx4 v[72:75], v134, s[100:101] nt
	global_load_dwordx4 v[76:79], v135, s[100:101] nt
	global_load_dwordx4 v[80:83], v136, s[100:101] nt
	global_load_dwordx4 v[84:87], v137, s[100:101] nt
	global_load_dwordx4 v[88:91], v138, s[100:101] nt
	global_load_dwordx4 v[92:95], v139, s[100:101] nt
	global_load_dwordx4 v[96:99], v140, s[100:101] nt
	global_load_dwordx4 v[100:103], v141, s[100:101] nt
	global_load_dwordx4 v[104:107], v142, s[100:101] nt
	global_load_dwordx4 v[108:111], v143, s[100:101] nt
	global_load_dwordx4 v[112:115], v144, s[100:101] nt
	global_load_dwordx4 v[116:119], v145, s[100:101] nt
	global_load_dwordx4 v[120:123], v146, s[100:101] nt
	global_load_dwordx4 v[124:127], v147, s[100:101] nt
	ds_write_b128 v148, v[152:155] offset:0
	ds_write_b128 v148, v[156:159] offset:128
	ds_write_b128 v149, v[160:163] offset:0
	ds_write_b128 v149, v[164:167] offset:128
	s_waitcnt lgkmcnt(0)
	s_barrier
	ds_read_b128 v[168:171], v150 offset:0
	ds_read_b128 v[172:175], v150 offset:1024
	ds_read_b128 v[176:179], v150 offset:2048
	ds_read_b128 v[180:183], v150 offset:3072
	s_waitcnt lgkmcnt(3)
	global_store_dwordx4 v150, v[168:171], s[6:7] nt
	s_waitcnt lgkmcnt(2)
	global_store_dwordx4 v150, v[172:175], s[6:7] offset:1024 nt
	s_waitcnt lgkmcnt(1)
	global_store_dwordx4 v150, v[176:179], s[6:7] offset:2048 nt
	s_waitcnt lgkmcnt(0)
	global_store_dwordx4 v150, v[180:183], s[6:7] offset:3072 nt
	s_add_u32 s6, s6, 0x8000
	s_addc_u32 s7, s7, 0
	s_waitcnt vmcnt(44)
	v_cvt_scalef32_pk_fp8_f32 v152, v184, v188, s5
	v_cvt_scalef32_pk_fp8_f32 v156, v185, v189, s5
	v_cvt_scalef32_pk_fp8_f32 v160, v186, v190, s5
	v_cvt_scalef32_pk_fp8_f32 v164, v187, v191, s5
	v_cvt_scalef32_pk_fp8_f32 v153, v200, v204, s5
	v_cvt_scalef32_pk_fp8_f32 v157, v201, v205, s5
	v_cvt_scalef32_pk_fp8_f32 v161, v202, v206, s5
	v_cvt_scalef32_pk_fp8_f32 v165, v203, v207, s5
	v_cvt_scalef32_pk_fp8_f32 v154, v216, v220, s5
	v_cvt_scalef32_pk_fp8_f32 v158, v217, v221, s5
	v_cvt_scalef32_pk_fp8_f32 v162, v218, v222, s5
	v_cvt_scalef32_pk_fp8_f32 v166, v219, v223, s5
	v_cvt_scalef32_pk_fp8_f32 v155, v232, v236, s5
	v_cvt_scalef32_pk_fp8_f32 v159, v233, v237, s5
	v_cvt_scalef32_pk_fp8_f32 v163, v234, v238, s5
	v_cvt_scalef32_pk_fp8_f32 v167, v235, v239, s5
	v_cvt_scalef32_pk_fp8_f32 v152, v192, v196, s5 op_sel:[0,0,0,1]
	v_cvt_scalef32_pk_fp8_f32 v156, v193, v197, s5 op_sel:[0,0,0,1]
	v_cvt_scalef32_pk_fp8_f32 v160, v194, v198, s5 op_sel:[0,0,0,1]
	v_cvt_scalef32_pk_fp8_f32 v164, v195, v199, s5 op_sel:[0,0,0,1]
	v_cvt_scalef32_pk_fp8_f32 v153, v208, v212, s5 op_sel:[0,0,0,1]
	v_cvt_scalef32_pk_fp8_f32 v157, v209, v213, s5 op_sel:[0,0,0,1]
	v_cvt_scalef32_pk_fp8_f32 v161, v210, v214, s5 op_sel:[0,0,0,1]
	v_cvt_scalef32_pk_fp8_f32 v165, v211, v215, s5 op_sel:[0,0,0,1]
	v_cvt_scalef32_pk_fp8_f32 v154, v224, v228, s5 op_sel:[0,0,0,1]
	v_cvt_scalef32_pk_fp8_f32 v158, v225, v229, s5 op_sel:[0,0,0,1]
	v_cvt_scalef32_pk_fp8_f32 v162, v226, v230, s5 op_sel:[0,0,0,1]
	v_cvt_scalef32_pk_fp8_f32 v166, v227, v231, s5 op_sel:[0,0,0,1]
	v_cvt_scalef32_pk_fp8_f32 v155, v240, v244, s5 op_sel:[0,0,0,1]
	v_cvt_scalef32_pk_fp8_f32 v159, v241, v245, s5 op_sel:[0,0,0,1]
	v_cvt_scalef32_pk_fp8_f32 v163, v242, v246, s5 op_sel:[0,0,0,1]
	v_cvt_scalef32_pk_fp8_f32 v167, v243, v247, s5 op_sel:[0,0,0,1]
	s_add_u32 s100, s100, s88
	s_addc_u32 s101, s101, 0
	global_load_dwordx4 v[184:187], v132, s[100:101] nt
	global_load_dwordx4 v[188:191], v133, s[100:101] nt
	global_load_dwordx4 v[192:195], v134, s[100:101] nt
	global_load_dwordx4 v[196:199], v135, s[100:101] nt
	global_load_dwordx4 v[200:203], v136, s[100:101] nt
	global_load_dwordx4 v[204:207], v137, s[100:101] nt
	global_load_dwordx4 v[208:211], v138, s[100:101] nt
	global_load_dwordx4 v[212:215], v139, s[100:101] nt
	global_load_dwordx4 v[216:219], v140, s[100:101] nt
	global_load_dwordx4 v[220:223], v141, s[100:101] nt
	global_load_dwordx4 v[224:227], v142, s[100:101] nt
	global_load_dwordx4 v[228:231], v143, s[100:101] nt
	global_load_dwordx4 v[232:235], v144, s[100:101] nt
	global_load_dwordx4 v[236:239], v145, s[100:101] nt
	global_load_dwordx4 v[240:243], v146, s[100:101] nt
	global_load_dwordx4 v[244:247], v147, s[100:101] nt
	ds_write_b128 v148, v[152:155] offset:32768
	ds_write_b128 v148, v[156:159] offset:32896
	ds_write_b128 v149, v[160:163] offset:32768
	ds_write_b128 v149, v[164:167] offset:32896
	s_waitcnt lgkmcnt(0)
	s_barrier
; #define G_SCHED __builtin_amdgcn_sched_barrier(0)
; #define CI_LOAD(R, kt) do { _Pragma("unroll") for (int _j = 0; _j < 16; ++_j) R[_j] = __builtin_nontemporal_load((const f32x4*)(src + (size_t)((kt) * 128 + _j) * LDB)); } while (0)
; template <int LDB>
; __device__ __forceinline__ void convert_image(const float* __restrict__ W, int col0, int col1, unsigned char* __restrict__ img, LAS3 char* lds, int wid) {
;     ...
;     f32x4 ra[16], rb[16];
;     CI_LOAD(ra, 0);
;     for (int kt = 0; kt < 16; kt += 2) {
;         CI_LOAD(rb, kt + 1); G_SCHED;
;         CI_CONV(ra, kt); G_SCHED;
;         CI_LOAD(ra, (kt + 2 < 16) ? kt + 2 : 15); G_SCHED;
	ds_read_b128 v[168:171], v150 offset:32768
	ds_read_b128 v[172:175], v150 offset:33792
	ds_read_b128 v[176:179], v150 offset:34816
	ds_read_b128 v[180:183], v150 offset:35840
	s_waitcnt lgkmcnt(3)
	global_store_dwordx4 v150, v[168:171], s[6:7] nt
	s_waitcnt lgkmcnt(2)
	global_store_dwordx4 v150, v[172:175], s[6:7] offset:1024 nt
	s_waitcnt lgkmcnt(1)
	global_store_dwordx4 v150, v[176:179], s[6:7] offset:2048 nt
	s_waitcnt lgkmcnt(0)
	global_store_dwordx4 v150, v[180:183], s[6:7] offset:3072 nt
	s_add_u32 s6, s6, 0x8000
	s_addc_u32 s7, s7, 0
	s_waitcnt vmcnt(44)
	v_cvt_scalef32_pk_fp8_f32 v152, v0, v4, s5
	v_cvt_scalef32_pk_fp8_f32 v156, v1, v5, s5
	v_cvt_scalef32_pk_fp8_f32 v160, v2, v6, s5
	v_cvt_scalef32_pk_fp8_f32 v164, v3, v7, s5
	v_cvt_scalef32_pk_fp8_f32 v153, v16, v20, s5
	v_cvt_scalef32_pk_fp8_f32 v157, v17, v21, s5
	v_cvt_scalef32_pk_fp8_f32 v161, v18, v22, s5
	v_cvt_scalef32_pk_fp8_f32 v165, v19, v23, s5
	v_cvt_scalef32_pk_fp8_f32 v154, v32, v36, s5
	v_cvt_scalef32_pk_fp8_f32 v158, v33, v37, s5
	v_cvt_scalef32_pk_fp8_f32 v162, v34, v38, s5
	v_cvt_scalef32_pk_fp8_f32 v166, v35, v39, s5
	v_cvt_scalef32_pk_fp8_f32 v155, v48, v52, s5
	v_cvt_scalef32_pk_fp8_f32 v159, v49, v53, s5
	v_cvt_scalef32_pk_fp8_f32 v163, v50, v54, s5
	v_cvt_scalef32_pk_fp8_f32 v167, v51, v55, s5
	v_cvt_scalef32_pk_fp8_f32 v152, v8, v12, s5 op_sel:[0,0,0,1]
	v_cvt_scalef32_pk_fp8_f32 v156, v9, v13, s5 op_sel:[0,0,0,1]
	v_cvt_scalef32_pk_fp8_f32 v160, v10, v14, s5 op_sel:[0,0,0,1]
	v_cvt_scalef32_pk_fp8_f32 v164, v11, v15, s5 op_sel:[0,0,0,1]
	v_cvt_scalef32_pk_fp8_f32 v153, v24, v28, s5 op_sel:[0,0,0,1]
	v_cvt_scalef32_pk_fp8_f32 v157, v25, v29, s5 op_sel:[0,0,0,1]
	v_cvt_scalef32_pk_fp8_f32 v161, v26, v30, s5 op_sel:[0,0,0,1]
	v_cvt_scalef32_pk_fp8_f32 v165, v27, v31, s5 op_sel:[0,0,0,1]
	v_cvt_scalef32_pk_fp8_f32 v154, v40, v44, s5 op_sel:[0,0,0,1]
	v_cvt_scalef32_pk_fp8_f32 v158, v41, v45, s5 op_sel:[0,0,0,1]
	v_cvt_scalef32_pk_fp8_f32 v162, v42, v46, s5 op_sel:[0,0,0,1]
	v_cvt_scalef32_pk_fp8_f32 v166, v43, v47, s5 op_sel:[0,0,0,1]
	v_cvt_scalef32_pk_fp8_f32 v155, v56, v60, s5 op_sel:[0,0,0,1]
	v_cvt_scalef32_pk_fp8_f32 v159, v57, v61, s5 op_sel:[0,0,0,1]
	v_cvt_scalef32_pk_fp8_f32 v163, v58, v62, s5 op_sel:[0,0,0,1]
	v_cvt_scalef32_pk_fp8_f32 v167, v59, v63, s5 op_sel:[0,0,0,1]
	s_add_u32 s100, s100, s88
	s_addc_u32 s101, s101, 0
	global_load_dwordx4 v[0:3], v132, s[100:101] nt
	global_load_dwordx4 v[4:7], v133, s[100:101] nt
	global_load_dwordx4 v[8:11], v134, s[100:101] nt
	global_load_dwordx4 v[12:15], v135, s[100:101] nt
	global_load_dwordx4 v[16:19], v136, s[100:101] nt
	global_load_dwordx4 v[20:23], v137, s[100:101] nt
	global_load_dwordx4 v[24:27], v138, s[100:101] nt
	global_load_dwordx4 v[28:31], v139, s[100:101] nt
	global_load_dwordx4 v[32:35], v140, s[100:101] nt
	global_load_dwordx4 v[36:39], v141, s[100:101] nt
	global_load_dwordx4 v[40:43], v142, s[100:101] nt
	global_load_dwordx4 v[44:47], v143, s[100:101] nt
	global_load_dwordx4 v[48:51], v144, s[100:101] nt
	global_load_dwordx4 v[52:55], v145, s[100:101] nt
	global_load_dwordx4 v[56:59], v146, s[100:101] nt
	global_load_dwordx4 v[60:63], v147, s[100:101] nt
	ds_write_b128 v148, v[152:155] offset:0
	ds_write_b128 v148, v[156:159] offset:128
	ds_write_b128 v149, v[160:163] offset:0
	ds_write_b128 v149, v[164:167] offset:128
	s_waitcnt lgkmcnt(0)
	s_barrier
	ds_read_b128 v[168:171], v150 offset:0
	ds_read_b128 v[172:175], v150 offset:1024
	ds_read_b128 v[176:179], v150 offset:2048
	ds_read_b128 v[180:183], v150 offset:3072
	s_waitcnt lgkmcnt(3)
	global_store_dwordx4 v150, v[168:171], s[6:7] nt
	s_waitcnt lgkmcnt(2)
	global_store_dwordx4 v150, v[172:175], s[6:7] offset:1024 nt
	s_waitcnt lgkmcnt(1)
	global_store_dwordx4 v150, v[176:179], s[6:7] offset:2048 nt
	s_waitcnt lgkmcnt(0)
	global_store_dwordx4 v150, v[180:183], s[6:7] offset:3072 nt
	s_add_u32 s6, s6, 0x8000
	s_addc_u32 s7, s7, 0
	s_waitcnt vmcnt(44)
	v_cvt_scalef32_pk_fp8_f32 v152, v64, v68, s5
	v_cvt_scalef32_pk_fp8_f32 v156, v65, v69, s5
	v_cvt_scalef32_pk_fp8_f32 v160, v66, v70, s5
	v_cvt_scalef32_pk_fp8_f32 v164, v67, v71, s5
	v_cvt_scalef32_pk_fp8_f32 v153, v80, v84, s5
	v_cvt_scalef32_pk_fp8_f32 v157, v81, v85, s5
	v_cvt_scalef32_pk_fp8_f32 v161, v82, v86, s5
	v_cvt_scalef32_pk_fp8_f32 v165, v83, v87, s5
	v_cvt_scalef32_pk_fp8_f32 v154, v96, v100, s5
	v_cvt_scalef32_pk_fp8_f32 v158, v97, v101, s5
	v_cvt_scalef32_pk_fp8_f32 v162, v98, v102, s5
	v_cvt_scalef32_pk_fp8_f32 v166, v99, v103, s5
	v_cvt_scalef32_pk_fp8_f32 v155, v112, v116, s5
	v_cvt_scalef32_pk_fp8_f32 v159, v113, v117, s5
	v_cvt_scalef32_pk_fp8_f32 v163, v114, v118, s5
	v_cvt_scalef32_pk_fp8_f32 v167, v115, v119, s5
	v_cvt_scalef32_pk_fp8_f32 v152, v72, v76, s5 op_sel:[0,0,0,1]
	v_cvt_scalef32_pk_fp8_f32 v156, v73, v77, s5 op_sel:[0,0,0,1]
	v_cvt_scalef32_pk_fp8_f32 v160, v74, v78, s5 op_sel:[0,0,0,1]
	v_cvt_scalef32_pk_fp8_f32 v164, v75, v79, s5 op_sel:[0,0,0,1]
	v_cvt_scalef32_pk_fp8_f32 v153, v88, v92, s5 op_sel:[0,0,0,1]
	v_cvt_scalef32_pk_fp8_f32 v157, v89, v93, s5 op_sel:[0,0,0,1]
	v_cvt_scalef32_pk_fp8_f32 v161, v90, v94, s5 op_sel:[0,0,0,1]
	v_cvt_scalef32_pk_fp8_f32 v165, v91, v95, s5 op_sel:[0,0,0,1]
	v_cvt_scalef32_pk_fp8_f32 v154, v104, v108, s5 op_sel:[0,0,0,1]
	v_cvt_scalef32_pk_fp8_f32 v158, v105, v109, s5 op_sel:[0,0,0,1]
	v_cvt_scalef32_pk_fp8_f32 v162, v106, v110, s5 op_sel:[0,0,0,1]
	v_cvt_scalef32_pk_fp8_f32 v166, v107, v111, s5 op_sel:[0,0,0,1]
	v_cvt_scalef32_pk_fp8_f32 v155, v120, v124, s5 op_sel:[0,0,0,1]
	v_cvt_scalef32_pk_fp8_f32 v159, v121, v125, s5 op_sel:[0,0,0,1]
	v_cvt_scalef32_pk_fp8_f32 v163, v122, v126, s5 op_sel:[0,0,0,1]
	v_cvt_scalef32_pk_fp8_f32 v167, v123, v127, s5 op_sel:[0,0,0,1]
	s_add_u32 s100, s100, s88
	s_addc_u32 s101, s101, 0
	global_load_dwordx4 v[64:67], v132, s[100:101] nt
	global_load_dwordx4 v[68:71], v133, s[100:101] nt
	global_load_dwordx4 v[72:75], v134, s[100:101] nt
	global_load_dwordx4 v[76:79], v135, s[100:101] nt
	global_load_dwordx4 v[80:83], v136, s[100:101] nt
	global_load_dwordx4 v[84:87], v137, s[100:101] nt
	global_load_dwordx4 v[88:91], v138, s[100:101] nt
	global_load_dwordx4 v[92:95], v139, s[100:101] nt
	global_load_dwordx4 v[96:99], v140, s[100:101] nt
	global_load_dwordx4 v[100:103], v141, s[100:101] nt
	global_load_dwordx4 v[104:107], v142, s[100:101] nt
	global_load_dwordx4 v[108:111], v143, s[100:101] nt
	global_load_dwordx4 v[112:115], v144, s[100:101] nt
	global_load_dwordx4 v[116:119], v145, s[100:101] nt
	global_load_dwordx4 v[120:123], v146, s[100:101] nt
	global_load_dwordx4 v[124:127], v147, s[100:101] nt
	ds_write_b128 v148, v[152:155] offset:32768
	ds_write_b128 v148, v[156:159] offset:32896
	ds_write_b128 v149, v[160:163] offset:32768
	ds_write_b128 v149, v[164:167] offset:32896
	s_waitcnt lgkmcnt(0)
	s_barrier
; #define G_SCHED __builtin_amdgcn_sched_barrier(0)
; #define CI_LOAD(R, kt) do { _Pragma("unroll") for (int _j = 0; _j < 16; ++_j) R[_j] = __builtin_nontemporal_load((const f32x4*)(src + (size_t)((kt) * 128 + _j) * LDB)); } while (0)
; template <int LDB>
; __device__ __forceinline__ void convert_image(const float* __restrict__ W, int col0, int col1, unsigned char* __restrict__ img, LAS3 char* lds, int wid) {
;     ...
;     f32x4 ra[16], rb[16];
;     CI_LOAD(ra, 0);
;     for (int kt = 0; kt < 16; kt += 2) {
;         CI_LOAD(rb, kt + 1); G_SCHED;
;         CI_CONV(ra, kt); G_SCHED;
;         CI_LOAD(ra, (kt + 2 < 16) ? kt + 2 : 15); G_SCHED;
	ds_read_b128 v[168:171], v150 offset:32768
	ds_read_b128 v[172:175], v150 offset:33792
	ds_read_b128 v[176:179], v150 offset:34816
	ds_read_b128 v[180:183], v150 offset:35840
	s_waitcnt lgkmcnt(3)
	global_store_dwordx4 v150, v[168:171], s[6:7] nt
	s_waitcnt lgkmcnt(2)
	global_store_dwordx4 v150, v[172:175], s[6:7] offset:1024 nt
	s_waitcnt lgkmcnt(1)
	global_store_dwordx4 v150, v[176:179], s[6:7] offset:2048 nt
	s_waitcnt lgkmcnt(0)
	global_store_dwordx4 v150, v[180:183], s[6:7] offset:3072 nt
	s_add_u32 s6, s6, 0x8000
	s_addc_u32 s7, s7, 0
	s_waitcnt vmcnt(44)
	v_cvt_scalef32_pk_fp8_f32 v152, v184, v188, s5
	v_cvt_scalef32_pk_fp8_f32 v156, v185, v189, s5
	v_cvt_scalef32_pk_fp8_f32 v160, v186, v190, s5
	v_cvt_scalef32_pk_fp8_f32 v164, v187, v191, s5
	v_cvt_scalef32_pk_fp8_f32 v153, v200, v204, s5
	v_cvt_scalef32_pk_fp8_f32 v157, v201, v205, s5
	v_cvt_scalef32_pk_fp8_f32 v161, v202, v206, s5
	v_cvt_scalef32_pk_fp8_f32 v165, v203, v207, s5
	v_cvt_scalef32_pk_fp8_f32 v154, v216, v220, s5
	v_cvt_scalef32_pk_fp8_f32 v158, v217, v221, s5
	v_cvt_scalef32_pk_fp8_f32 v162, v218, v222, s5
	v_cvt_scalef32_pk_fp8_f32 v166, v219, v223, s5
	v_cvt_scalef32_pk_fp8_f32 v155, v232, v236, s5
	v_cvt_scalef32_pk_fp8_f32 v159, v233, v237, s5
	v_cvt_scalef32_pk_fp8_f32 v163, v234, v238, s5
	v_cvt_scalef32_pk_fp8_f32 v167, v235, v239, s5
	v_cvt_scalef32_pk_fp8_f32 v152, v192, v196, s5 op_sel:[0,0,0,1]
	v_cvt_scalef32_pk_fp8_f32 v156, v193, v197, s5 op_sel:[0,0,0,1]
	v_cvt_scalef32_pk_fp8_f32 v160, v194, v198, s5 op_sel:[0,0,0,1]
	v_cvt_scalef32_pk_fp8_f32 v164, v195, v199, s5 op_sel:[0,0,0,1]
	v_cvt_scalef32_pk_fp8_f32 v153, v208, v212, s5 op_sel:[0,0,0,1]
	v_cvt_scalef32_pk_fp8_f32 v157, v209, v213, s5 op_sel:[0,0,0,1]
	v_cvt_scalef32_pk_fp8_f32 v161, v210, v214, s5 op_sel:[0,0,0,1]
	v_cvt_scalef32_pk_fp8_f32 v165, v211, v215, s5 op_sel:[0,0,0,1]
	v_cvt_scalef32_pk_fp8_f32 v154, v224, v228, s5 op_sel:[0,0,0,1]
	v_cvt_scalef32_pk_fp8_f32 v158, v225, v229, s5 op_sel:[0,0,0,1]
	v_cvt_scalef32_pk_fp8_f32 v162, v226, v230, s5 op_sel:[0,0,0,1]
	v_cvt_scalef32_pk_fp8_f32 v166, v227, v231, s5 op_sel:[0,0,0,1]
	v_cvt_scalef32_pk_fp8_f32 v155, v240, v244, s5 op_sel:[0,0,0,1]
	v_cvt_scalef32_pk_fp8_f32 v159, v241, v245, s5 op_sel:[0,0,0,1]
	v_cvt_scalef32_pk_fp8_f32 v163, v242, v246, s5 op_sel:[0,0,0,1]
	v_cvt_scalef32_pk_fp8_f32 v167, v243, v247, s5 op_sel:[0,0,0,1]
	s_add_u32 s100, s100, s88
	s_addc_u32 s101, s101, 0
	global_load_dwordx4 v[184:187], v132, s[100:101] nt
	global_load_dwordx4 v[188:191], v133, s[100:101] nt
	global_load_dwordx4 v[192:195], v134, s[100:101] nt
	global_load_dwordx4 v[196:199], v135, s[100:101] nt
	global_load_dwordx4 v[200:203], v136, s[100:101] nt
	global_load_dwordx4 v[204:207], v137, s[100:101] nt
	global_load_dwordx4 v[208:211], v138, s[100:101] nt
	global_load_dwordx4 v[212:215], v139, s[100:101] nt
	global_load_dwordx4 v[216:219], v140, s[100:101] nt
	global_load_dwordx4 v[220:223], v141, s[100:101] nt
	global_load_dwordx4 v[224:227], v142, s[100:101] nt
	global_load_dwordx4 v[228:231], v143, s[100:101] nt
	global_load_dwordx4 v[232:235], v144, s[100:101] nt
	global_load_dwordx4 v[236:239], v145, s[100:101] nt
	global_load_dwordx4 v[240:243], v146, s[100:101] nt
	global_load_dwordx4 v[244:247], v147, s[100:101] nt
	ds_write_b128 v148, v[152:155] offset:0
	ds_write_b128 v148, v[156:159] offset:128
	ds_write_b128 v149, v[160:163] offset:0
	ds_write_b128 v149, v[164:167] offset:128
	s_waitcnt lgkmcnt(0)
	s_barrier
	ds_read_b128 v[168:171], v150 offset:0
	ds_read_b128 v[172:175], v150 offset:1024
	ds_read_b128 v[176:179], v150 offset:2048
	ds_read_b128 v[180:183], v150 offset:3072
	s_waitcnt lgkmcnt(3)
	global_store_dwordx4 v150, v[168:171], s[6:7] nt
	s_waitcnt lgkmcnt(2)
	global_store_dwordx4 v150, v[172:175], s[6:7] offset:1024 nt
	s_waitcnt lgkmcnt(1)
	global_store_dwordx4 v150, v[176:179], s[6:7] offset:2048 nt
	s_waitcnt lgkmcnt(0)
	global_store_dwordx4 v150, v[180:183], s[6:7] offset:3072 nt
	s_add_u32 s6, s6, 0x8000
	s_addc_u32 s7, s7, 0
	s_waitcnt vmcnt(44)
	v_cvt_scalef32_pk_fp8_f32 v152, v0, v4, s5
	v_cvt_scalef32_pk_fp8_f32 v156, v1, v5, s5
	v_cvt_scalef32_pk_fp8_f32 v160, v2, v6, s5
	v_cvt_scalef32_pk_fp8_f32 v164, v3, v7, s5
	v_cvt_scalef32_pk_fp8_f32 v153, v16, v20, s5
	v_cvt_scalef32_pk_fp8_f32 v157, v17, v21, s5
	v_cvt_scalef32_pk_fp8_f32 v161, v18, v22, s5
	v_cvt_scalef32_pk_fp8_f32 v165, v19, v23, s5
	v_cvt_scalef32_pk_fp8_f32 v154, v32, v36, s5
	v_cvt_scalef32_pk_fp8_f32 v158, v33, v37, s5
	v_cvt_scalef32_pk_fp8_f32 v162, v34, v38, s5
	v_cvt_scalef32_pk_fp8_f32 v166, v35, v39, s5
	v_cvt_scalef32_pk_fp8_f32 v155, v48, v52, s5
	v_cvt_scalef32_pk_fp8_f32 v159, v49, v53, s5
	v_cvt_scalef32_pk_fp8_f32 v163, v50, v54, s5
	v_cvt_scalef32_pk_fp8_f32 v167, v51, v55, s5
	v_cvt_scalef32_pk_fp8_f32 v152, v8, v12, s5 op_sel:[0,0,0,1]
	v_cvt_scalef32_pk_fp8_f32 v156, v9, v13, s5 op_sel:[0,0,0,1]
	v_cvt_scalef32_pk_fp8_f32 v160, v10, v14, s5 op_sel:[0,0,0,1]
	v_cvt_scalef32_pk_fp8_f32 v164, v11, v15, s5 op_sel:[0,0,0,1]
	v_cvt_scalef32_pk_fp8_f32 v153, v24, v28, s5 op_sel:[0,0,0,1]
	v_cvt_scalef32_pk_fp8_f32 v157, v25, v29, s5 op_sel:[0,0,0,1]
	v_cvt_scalef32_pk_fp8_f32 v161, v26, v30, s5 op_sel:[0,0,0,1]
	v_cvt_scalef32_pk_fp8_f32 v165, v27, v31, s5 op_sel:[0,0,0,1]
	v_cvt_scalef32_pk_fp8_f32 v154, v40, v44, s5 op_sel:[0,0,0,1]
	v_cvt_scalef32_pk_fp8_f32 v158, v41, v45, s5 op_sel:[0,0,0,1]
	v_cvt_scalef32_pk_fp8_f32 v162, v42, v46, s5 op_sel:[0,0,0,1]
	v_cvt_scalef32_pk_fp8_f32 v166, v43, v47, s5 op_sel:[0,0,0,1]
	v_cvt_scalef32_pk_fp8_f32 v155, v56, v60, s5 op_sel:[0,0,0,1]
	v_cvt_scalef32_pk_fp8_f32 v159, v57, v61, s5 op_sel:[0,0,0,1]
	v_cvt_scalef32_pk_fp8_f32 v163, v58, v62, s5 op_sel:[0,0,0,1]
	v_cvt_scalef32_pk_fp8_f32 v167, v59, v63, s5 op_sel:[0,0,0,1]
	s_add_u32 s100, s100, s88
	s_addc_u32 s101, s101, 0
	global_load_dwordx4 v[0:3], v132, s[100:101] nt
	global_load_dwordx4 v[4:7], v133, s[100:101] nt
	global_load_dwordx4 v[8:11], v134, s[100:101] nt
	global_load_dwordx4 v[12:15], v135, s[100:101] nt
	global_load_dwordx4 v[16:19], v136, s[100:101] nt
	global_load_dwordx4 v[20:23], v137, s[100:101] nt
	global_load_dwordx4 v[24:27], v138, s[100:101] nt
	global_load_dwordx4 v[28:31], v139, s[100:101] nt
	global_load_dwordx4 v[32:35], v140, s[100:101] nt
	global_load_dwordx4 v[36:39], v141, s[100:101] nt
	global_load_dwordx4 v[40:43], v142, s[100:101] nt
	global_load_dwordx4 v[44:47], v143, s[100:101] nt
	global_load_dwordx4 v[48:51], v144, s[100:101] nt
	global_load_dwordx4 v[52:55], v145, s[100:101] nt
	global_load_dwordx4 v[56:59], v146, s[100:101] nt
	global_load_dwordx4 v[60:63], v147, s[100:101] nt
	ds_write_b128 v148, v[152:155] offset:32768
	ds_write_b128 v148, v[156:159] offset:32896
	ds_write_b128 v149, v[160:163] offset:32768
	ds_write_b128 v149, v[164:167] offset:32896
	s_waitcnt lgkmcnt(0)
	s_barrier
; #define G_SCHED __builtin_amdgcn_sched_barrier(0)
; #define CI_LOAD(R, kt) do { _Pragma("unroll") for (int _j = 0; _j < 16; ++_j) R[_j] = __builtin_nontemporal_load((const f32x4*)(src + (size_t)((kt) * 128 + _j) * LDB)); } while (0)
; template <int LDB>
; __device__ __forceinline__ void convert_image(const float* __restrict__ W, int col0, int col1, unsigned char* __restrict__ img, LAS3 char* lds, int wid) {
;     ...
;     f32x4 ra[16], rb[16];
;     CI_LOAD(ra, 0);
;     for (int kt = 0; kt < 16; kt += 2) {
;         CI_LOAD(rb, kt + 1); G_SCHED;
;         CI_CONV(ra, kt); G_SCHED;
;         CI_LOAD(ra, (kt + 2 < 16) ? kt + 2 : 15); G_SCHED;
	ds_read_b128 v[168:171], v150 offset:32768
	ds_read_b128 v[172:175], v150 offset:33792
	ds_read_b128 v[176:179], v150 offset:34816
	ds_read_b128 v[180:183], v150 offset:35840
	s_waitcnt lgkmcnt(3)
	global_store_dwordx4 v150, v[168:171], s[6:7] nt
	s_waitcnt lgkmcnt(2)
	global_store_dwordx4 v150, v[172:175], s[6:7] offset:1024 nt
	s_waitcnt lgkmcnt(1)
	global_store_dwordx4 v150, v[176:179], s[6:7] offset:2048 nt
	s_waitcnt lgkmcnt(0)
	global_store_dwordx4 v150, v[180:183], s[6:7] offset:3072 nt
	s_add_u32 s6, s6, 0x8000
	s_addc_u32 s7, s7, 0
	s_waitcnt vmcnt(44)
	v_cvt_scalef32_pk_fp8_f32 v152, v64, v68, s5
	v_cvt_scalef32_pk_fp8_f32 v156, v65, v69, s5
	v_cvt_scalef32_pk_fp8_f32 v160, v66, v70, s5
	v_cvt_scalef32_pk_fp8_f32 v164, v67, v71, s5
	v_cvt_scalef32_pk_fp8_f32 v153, v80, v84, s5
	v_cvt_scalef32_pk_fp8_f32 v157, v81, v85, s5
	v_cvt_scalef32_pk_fp8_f32 v161, v82, v86, s5
	v_cvt_scalef32_pk_fp8_f32 v165, v83, v87, s5
	v_cvt_scalef32_pk_fp8_f32 v154, v96, v100, s5
	v_cvt_scalef32_pk_fp8_f32 v158, v97, v101, s5
	v_cvt_scalef32_pk_fp8_f32 v162, v98, v102, s5
	v_cvt_scalef32_pk_fp8_f32 v166, v99, v103, s5
	v_cvt_scalef32_pk_fp8_f32 v155, v112, v116, s5
	v_cvt_scalef32_pk_fp8_f32 v159, v113, v117, s5
	v_cvt_scalef32_pk_fp8_f32 v163, v114, v118, s5
	v_cvt_scalef32_pk_fp8_f32 v167, v115, v119, s5
	v_cvt_scalef32_pk_fp8_f32 v152, v72, v76, s5 op_sel:[0,0,0,1]
	v_cvt_scalef32_pk_fp8_f32 v156, v73, v77, s5 op_sel:[0,0,0,1]
	v_cvt_scalef32_pk_fp8_f32 v160, v74, v78, s5 op_sel:[0,0,0,1]
	v_cvt_scalef32_pk_fp8_f32 v164, v75, v79, s5 op_sel:[0,0,0,1]
	v_cvt_scalef32_pk_fp8_f32 v153, v88, v92, s5 op_sel:[0,0,0,1]
	v_cvt_scalef32_pk_fp8_f32 v157, v89, v93, s5 op_sel:[0,0,0,1]
	v_cvt_scalef32_pk_fp8_f32 v161, v90, v94, s5 op_sel:[0,0,0,1]
	v_cvt_scalef32_pk_fp8_f32 v165, v91, v95, s5 op_sel:[0,0,0,1]
	v_cvt_scalef32_pk_fp8_f32 v154, v104, v108, s5 op_sel:[0,0,0,1]
	v_cvt_scalef32_pk_fp8_f32 v158, v105, v109, s5 op_sel:[0,0,0,1]
	v_cvt_scalef32_pk_fp8_f32 v162, v106, v110, s5 op_sel:[0,0,0,1]
	v_cvt_scalef32_pk_fp8_f32 v166, v107, v111, s5 op_sel:[0,0,0,1]
	v_cvt_scalef32_pk_fp8_f32 v155, v120, v124, s5 op_sel:[0,0,0,1]
	v_cvt_scalef32_pk_fp8_f32 v159, v121, v125, s5 op_sel:[0,0,0,1]
	v_cvt_scalef32_pk_fp8_f32 v163, v122, v126, s5 op_sel:[0,0,0,1]
	v_cvt_scalef32_pk_fp8_f32 v167, v123, v127, s5 op_sel:[0,0,0,1]
	s_add_u32 s100, s100, s88
	s_addc_u32 s101, s101, 0
	global_load_dwordx4 v[64:67], v132, s[100:101] nt
	global_load_dwordx4 v[68:71], v133, s[100:101] nt
	global_load_dwordx4 v[72:75], v134, s[100:101] nt
	global_load_dwordx4 v[76:79], v135, s[100:101] nt
	global_load_dwordx4 v[80:83], v136, s[100:101] nt
	global_load_dwordx4 v[84:87], v137, s[100:101] nt
	global_load_dwordx4 v[88:91], v138, s[100:101] nt
	global_load_dwordx4 v[92:95], v139, s[100:101] nt
	global_load_dwordx4 v[96:99], v140, s[100:101] nt
	global_load_dwordx4 v[100:103], v141, s[100:101] nt
	global_load_dwordx4 v[104:107], v142, s[100:101] nt
	global_load_dwordx4 v[108:111], v143, s[100:101] nt
	global_load_dwordx4 v[112:115], v144, s[100:101] nt
	global_load_dwordx4 v[116:119], v145, s[100:101] nt
	global_load_dwordx4 v[120:123], v146, s[100:101] nt
	global_load_dwordx4 v[124:127], v147, s[100:101] nt
	ds_write_b128 v148, v[152:155] offset:0
	ds_write_b128 v148, v[156:159] offset:128
	ds_write_b128 v149, v[160:163] offset:0
	ds_write_b128 v149, v[164:167] offset:128
	s_waitcnt lgkmcnt(0)
	s_barrier
	ds_read_b128 v[168:171], v150 offset:0
	ds_read_b128 v[172:175], v150 offset:1024
	ds_read_b128 v[176:179], v150 offset:2048
	ds_read_b128 v[180:183], v150 offset:3072
	s_waitcnt lgkmcnt(3)
	global_store_dwordx4 v150, v[168:171], s[6:7] nt
	s_waitcnt lgkmcnt(2)
	global_store_dwordx4 v150, v[172:175], s[6:7] offset:1024 nt
	s_waitcnt lgkmcnt(1)
	global_store_dwordx4 v150, v[176:179], s[6:7] offset:2048 nt
	s_waitcnt lgkmcnt(0)
	global_store_dwordx4 v150, v[180:183], s[6:7] offset:3072 nt
	s_add_u32 s6, s6, 0x8000
	s_addc_u32 s7, s7, 0
	s_waitcnt vmcnt(44)
	v_cvt_scalef32_pk_fp8_f32 v152, v184, v188, s5
	v_cvt_scalef32_pk_fp8_f32 v156, v185, v189, s5
	v_cvt_scalef32_pk_fp8_f32 v160, v186, v190, s5
	v_cvt_scalef32_pk_fp8_f32 v164, v187, v191, s5
	v_cvt_scalef32_pk_fp8_f32 v153, v200, v204, s5
	v_cvt_scalef32_pk_fp8_f32 v157, v201, v205, s5
	v_cvt_scalef32_pk_fp8_f32 v161, v202, v206, s5
	v_cvt_scalef32_pk_fp8_f32 v165, v203, v207, s5
	v_cvt_scalef32_pk_fp8_f32 v154, v216, v220, s5
	v_cvt_scalef32_pk_fp8_f32 v158, v217, v221, s5
	v_cvt_scalef32_pk_fp8_f32 v162, v218, v222, s5
	v_cvt_scalef32_pk_fp8_f32 v166, v219, v223, s5
	v_cvt_scalef32_pk_fp8_f32 v155, v232, v236, s5
	v_cvt_scalef32_pk_fp8_f32 v159, v233, v237, s5
	v_cvt_scalef32_pk_fp8_f32 v163, v234, v238, s5
	v_cvt_scalef32_pk_fp8_f32 v167, v235, v239, s5
	v_cvt_scalef32_pk_fp8_f32 v152, v192, v196, s5 op_sel:[0,0,0,1]
	v_cvt_scalef32_pk_fp8_f32 v156, v193, v197, s5 op_sel:[0,0,0,1]
	v_cvt_scalef32_pk_fp8_f32 v160, v194, v198, s5 op_sel:[0,0,0,1]
	v_cvt_scalef32_pk_fp8_f32 v164, v195, v199, s5 op_sel:[0,0,0,1]
	v_cvt_scalef32_pk_fp8_f32 v153, v208, v212, s5 op_sel:[0,0,0,1]
	v_cvt_scalef32_pk_fp8_f32 v157, v209, v213, s5 op_sel:[0,0,0,1]
	v_cvt_scalef32_pk_fp8_f32 v161, v210, v214, s5 op_sel:[0,0,0,1]
	v_cvt_scalef32_pk_fp8_f32 v165, v211, v215, s5 op_sel:[0,0,0,1]
	v_cvt_scalef32_pk_fp8_f32 v154, v224, v228, s5 op_sel:[0,0,0,1]
	v_cvt_scalef32_pk_fp8_f32 v158, v225, v229, s5 op_sel:[0,0,0,1]
	v_cvt_scalef32_pk_fp8_f32 v162, v226, v230, s5 op_sel:[0,0,0,1]
	v_cvt_scalef32_pk_fp8_f32 v166, v227, v231, s5 op_sel:[0,0,0,1]
	v_cvt_scalef32_pk_fp8_f32 v155, v240, v244, s5 op_sel:[0,0,0,1]
	v_cvt_scalef32_pk_fp8_f32 v159, v241, v245, s5 op_sel:[0,0,0,1]
	v_cvt_scalef32_pk_fp8_f32 v163, v242, v246, s5 op_sel:[0,0,0,1]
	v_cvt_scalef32_pk_fp8_f32 v167, v243, v247, s5 op_sel:[0,0,0,1]
	s_add_u32 s100, s100, s88
	s_addc_u32 s101, s101, 0
	global_load_dwordx4 v[184:187], v132, s[100:101] nt
	global_load_dwordx4 v[188:191], v133, s[100:101] nt
	global_load_dwordx4 v[192:195], v134, s[100:101] nt
	global_load_dwordx4 v[196:199], v135, s[100:101] nt
	global_load_dwordx4 v[200:203], v136, s[100:101] nt
	global_load_dwordx4 v[204:207], v137, s[100:101] nt
	global_load_dwordx4 v[208:211], v138, s[100:101] nt
	global_load_dwordx4 v[212:215], v139, s[100:101] nt
	global_load_dwordx4 v[216:219], v140, s[100:101] nt
	global_load_dwordx4 v[220:223], v141, s[100:101] nt
	global_load_dwordx4 v[224:227], v142, s[100:101] nt
	global_load_dwordx4 v[228:231], v143, s[100:101] nt
	global_load_dwordx4 v[232:235], v144, s[100:101] nt
	global_load_dwordx4 v[236:239], v145, s[100:101] nt
	global_load_dwordx4 v[240:243], v146, s[100:101] nt
	global_load_dwordx4 v[244:247], v147, s[100:101] nt
	ds_write_b128 v148, v[152:155] offset:32768
	ds_write_b128 v148, v[156:159] offset:32896
	ds_write_b128 v149, v[160:163] offset:32768
	ds_write_b128 v149, v[164:167] offset:32896
	s_waitcnt lgkmcnt(0)
	s_barrier
; #define G_SCHED __builtin_amdgcn_sched_barrier(0)
; #define CI_LOAD(R, kt) do { _Pragma("unroll") for (int _j = 0; _j < 16; ++_j) R[_j] = __builtin_nontemporal_load((const f32x4*)(src + (size_t)((kt) * 128 + _j) * LDB)); } while (0)
; template <int LDB>
; __device__ __forceinline__ void convert_image(const float* __restrict__ W, int col0, int col1, unsigned char* __restrict__ img, LAS3 char* lds, int wid) {
;     ...
;     f32x4 ra[16], rb[16];
;     CI_LOAD(ra, 0);
;     for (int kt = 0; kt < 16; kt += 2) {
;         CI_LOAD(rb, kt + 1); G_SCHED;
;         CI_CONV(ra, kt); G_SCHED;
;         CI_LOAD(ra, (kt + 2 < 16) ? kt + 2 : 15); G_SCHED;
	ds_read_b128 v[168:171], v150 offset:32768
	ds_read_b128 v[172:175], v150 offset:33792
	ds_read_b128 v[176:179], v150 offset:34816
	ds_read_b128 v[180:183], v150 offset:35840
	s_waitcnt lgkmcnt(3)
	global_store_dwordx4 v150, v[168:171], s[6:7] nt
	s_waitcnt lgkmcnt(2)
	global_store_dwordx4 v150, v[172:175], s[6:7] offset:1024 nt
	s_waitcnt lgkmcnt(1)
	global_store_dwordx4 v150, v[176:179], s[6:7] offset:2048 nt
	s_waitcnt lgkmcnt(0)
	global_store_dwordx4 v150, v[180:183], s[6:7] offset:3072 nt
	s_add_u32 s6, s6, 0x8000
	s_addc_u32 s7, s7, 0
	s_waitcnt vmcnt(44)
	v_cvt_scalef32_pk_fp8_f32 v152, v0, v4, s5
	v_cvt_scalef32_pk_fp8_f32 v156, v1, v5, s5
	v_cvt_scalef32_pk_fp8_f32 v160, v2, v6, s5
	v_cvt_scalef32_pk_fp8_f32 v164, v3, v7, s5
	v_cvt_scalef32_pk_fp8_f32 v153, v16, v20, s5
	v_cvt_scalef32_pk_fp8_f32 v157, v17, v21, s5
	v_cvt_scalef32_pk_fp8_f32 v161, v18, v22, s5
	v_cvt_scalef32_pk_fp8_f32 v165, v19, v23, s5
	v_cvt_scalef32_pk_fp8_f32 v154, v32, v36, s5
	v_cvt_scalef32_pk_fp8_f32 v158, v33, v37, s5
	v_cvt_scalef32_pk_fp8_f32 v162, v34, v38, s5
	v_cvt_scalef32_pk_fp8_f32 v166, v35, v39, s5
	v_cvt_scalef32_pk_fp8_f32 v155, v48, v52, s5
	v_cvt_scalef32_pk_fp8_f32 v159, v49, v53, s5
	v_cvt_scalef32_pk_fp8_f32 v163, v50, v54, s5
	v_cvt_scalef32_pk_fp8_f32 v167, v51, v55, s5
	v_cvt_scalef32_pk_fp8_f32 v152, v8, v12, s5 op_sel:[0,0,0,1]
	v_cvt_scalef32_pk_fp8_f32 v156, v9, v13, s5 op_sel:[0,0,0,1]
	v_cvt_scalef32_pk_fp8_f32 v160, v10, v14, s5 op_sel:[0,0,0,1]
	v_cvt_scalef32_pk_fp8_f32 v164, v11, v15, s5 op_sel:[0,0,0,1]
	v_cvt_scalef32_pk_fp8_f32 v153, v24, v28, s5 op_sel:[0,0,0,1]
	v_cvt_scalef32_pk_fp8_f32 v157, v25, v29, s5 op_sel:[0,0,0,1]
	v_cvt_scalef32_pk_fp8_f32 v161, v26, v30, s5 op_sel:[0,0,0,1]
	v_cvt_scalef32_pk_fp8_f32 v165, v27, v31, s5 op_sel:[0,0,0,1]
	v_cvt_scalef32_pk_fp8_f32 v154, v40, v44, s5 op_sel:[0,0,0,1]
	v_cvt_scalef32_pk_fp8_f32 v158, v41, v45, s5 op_sel:[0,0,0,1]
	v_cvt_scalef32_pk_fp8_f32 v162, v42, v46, s5 op_sel:[0,0,0,1]
	v_cvt_scalef32_pk_fp8_f32 v166, v43, v47, s5 op_sel:[0,0,0,1]
	v_cvt_scalef32_pk_fp8_f32 v155, v56, v60, s5 op_sel:[0,0,0,1]
	v_cvt_scalef32_pk_fp8_f32 v159, v57, v61, s5 op_sel:[0,0,0,1]
	v_cvt_scalef32_pk_fp8_f32 v163, v58, v62, s5 op_sel:[0,0,0,1]
	v_cvt_scalef32_pk_fp8_f32 v167, v59, v63, s5 op_sel:[0,0,0,1]
	s_add_u32 s100, s100, s88
	s_addc_u32 s101, s101, 0
	global_load_dwordx4 v[0:3], v132, s[100:101] nt
	global_load_dwordx4 v[4:7], v133, s[100:101] nt
	global_load_dwordx4 v[8:11], v134, s[100:101] nt
	global_load_dwordx4 v[12:15], v135, s[100:101] nt
	global_load_dwordx4 v[16:19], v136, s[100:101] nt
	global_load_dwordx4 v[20:23], v137, s[100:101] nt
	global_load_dwordx4 v[24:27], v138, s[100:101] nt
	global_load_dwordx4 v[28:31], v139, s[100:101] nt
	global_load_dwordx4 v[32:35], v140, s[100:101] nt
	global_load_dwordx4 v[36:39], v141, s[100:101] nt
	global_load_dwordx4 v[40:43], v142, s[100:101] nt
	global_load_dwordx4 v[44:47], v143, s[100:101] nt
	global_load_dwordx4 v[48:51], v144, s[100:101] nt
	global_load_dwordx4 v[52:55], v145, s[100:101] nt
	global_load_dwordx4 v[56:59], v146, s[100:101] nt
	global_load_dwordx4 v[60:63], v147, s[100:101] nt
	ds_write_b128 v148, v[152:155] offset:0
	ds_write_b128 v148, v[156:159] offset:128
	ds_write_b128 v149, v[160:163] offset:0
	ds_write_b128 v149, v[164:167] offset:128
	s_waitcnt lgkmcnt(0)
	s_barrier
	ds_read_b128 v[168:171], v150 offset:0
	ds_read_b128 v[172:175], v150 offset:1024
	ds_read_b128 v[176:179], v150 offset:2048
	ds_read_b128 v[180:183], v150 offset:3072
	s_waitcnt lgkmcnt(3)
	global_store_dwordx4 v150, v[168:171], s[6:7] nt
	s_waitcnt lgkmcnt(2)
	global_store_dwordx4 v150, v[172:175], s[6:7] offset:1024 nt
	s_waitcnt lgkmcnt(1)
	global_store_dwordx4 v150, v[176:179], s[6:7] offset:2048 nt
	s_waitcnt lgkmcnt(0)
	global_store_dwordx4 v150, v[180:183], s[6:7] offset:3072 nt
	s_add_u32 s6, s6, 0x8000
	s_addc_u32 s7, s7, 0
	s_waitcnt vmcnt(44)
	v_cvt_scalef32_pk_fp8_f32 v152, v64, v68, s5
	v_cvt_scalef32_pk_fp8_f32 v156, v65, v69, s5
	v_cvt_scalef32_pk_fp8_f32 v160, v66, v70, s5
	v_cvt_scalef32_pk_fp8_f32 v164, v67, v71, s5
	v_cvt_scalef32_pk_fp8_f32 v153, v80, v84, s5
	v_cvt_scalef32_pk_fp8_f32 v157, v81, v85, s5
	v_cvt_scalef32_pk_fp8_f32 v161, v82, v86, s5
	v_cvt_scalef32_pk_fp8_f32 v165, v83, v87, s5
	v_cvt_scalef32_pk_fp8_f32 v154, v96, v100, s5
	v_cvt_scalef32_pk_fp8_f32 v158, v97, v101, s5
	v_cvt_scalef32_pk_fp8_f32 v162, v98, v102, s5
	v_cvt_scalef32_pk_fp8_f32 v166, v99, v103, s5
	v_cvt_scalef32_pk_fp8_f32 v155, v112, v116, s5
	v_cvt_scalef32_pk_fp8_f32 v159, v113, v117, s5
	v_cvt_scalef32_pk_fp8_f32 v163, v114, v118, s5
	v_cvt_scalef32_pk_fp8_f32 v167, v115, v119, s5
	v_cvt_scalef32_pk_fp8_f32 v152, v72, v76, s5 op_sel:[0,0,0,1]
	v_cvt_scalef32_pk_fp8_f32 v156, v73, v77, s5 op_sel:[0,0,0,1]
	v_cvt_scalef32_pk_fp8_f32 v160, v74, v78, s5 op_sel:[0,0,0,1]
	v_cvt_scalef32_pk_fp8_f32 v164, v75, v79, s5 op_sel:[0,0,0,1]
	v_cvt_scalef32_pk_fp8_f32 v153, v88, v92, s5 op_sel:[0,0,0,1]
	v_cvt_scalef32_pk_fp8_f32 v157, v89, v93, s5 op_sel:[0,0,0,1]
	v_cvt_scalef32_pk_fp8_f32 v161, v90, v94, s5 op_sel:[0,0,0,1]
	v_cvt_scalef32_pk_fp8_f32 v165, v91, v95, s5 op_sel:[0,0,0,1]
	v_cvt_scalef32_pk_fp8_f32 v154, v104, v108, s5 op_sel:[0,0,0,1]
	v_cvt_scalef32_pk_fp8_f32 v158, v105, v109, s5 op_sel:[0,0,0,1]
	v_cvt_scalef32_pk_fp8_f32 v162, v106, v110, s5 op_sel:[0,0,0,1]
	v_cvt_scalef32_pk_fp8_f32 v166, v107, v111, s5 op_sel:[0,0,0,1]
	v_cvt_scalef32_pk_fp8_f32 v155, v120, v124, s5 op_sel:[0,0,0,1]
	v_cvt_scalef32_pk_fp8_f32 v159, v121, v125, s5 op_sel:[0,0,0,1]
	v_cvt_scalef32_pk_fp8_f32 v163, v122, v126, s5 op_sel:[0,0,0,1]
	v_cvt_scalef32_pk_fp8_f32 v167, v123, v127, s5 op_sel:[0,0,0,1]
	ds_write_b128 v148, v[152:155] offset:32768
	ds_write_b128 v148, v[156:159] offset:32896
	ds_write_b128 v149, v[160:163] offset:32768
	ds_write_b128 v149, v[164:167] offset:32896
	s_waitcnt lgkmcnt(0)
	s_barrier
; #define G_SCHED __builtin_amdgcn_sched_barrier(0)
; #define CI_LOAD(R, kt) do { _Pragma("unroll") for (int _j = 0; _j < 16; ++_j) R[_j] = __builtin_nontemporal_load((const f32x4*)(src + (size_t)((kt) * 128 + _j) * LDB)); } while (0)
; #define LD_WAIT(r) asm volatile("s_waitcnt vmcnt(0)" : "+v"(r) :: "memory")
; template <int LDB>
; __device__ __forceinline__ void convert_image(const float* __restrict__ W, int col0, int col1, unsigned char* __restrict__ img, LAS3 char* lds, int wid) {
;     ...
;     f32x4 ra[16], rb[16];
;     CI_LOAD(ra, 0);
;     for (int kt = 0; kt < 16; kt += 2) {
;         CI_LOAD(rb, kt + 1); G_SCHED;
;         CI_CONV(ra, kt); G_SCHED;
;         CI_LOAD(ra, (kt + 2 < 16) ? kt + 2 : 15); G_SCHED;
;         CI_CONV(rb, kt + 1); G_SCHED;
;     }
;     asm volatile("s_waitcnt vmcnt(0)" ::: "memory");
;     __syncthreads();
; template <int EPI>
; __device__ __forceinline__ int* moe_phase(const Params& p, LAS3 char* lds, int wid, int* pend_in) {
;     ...
;                         if (t0 == 0) { __hip_atomic_store(sy.flag, 1, __ATOMIC_RELAXED, __HIP_MEMORY_SCOPE_AGENT); unsigned c0 = inc_early(&qctr[qq]); LD_WAIT(c0); slot[par ^ 1] = ((unsigned)qq << 20) | c0; }
	ds_read_b128 v[168:171], v150 offset:32768
	ds_read_b128 v[172:175], v150 offset:33792
	ds_read_b128 v[176:179], v150 offset:34816
	ds_read_b128 v[180:183], v150 offset:35840
	s_waitcnt lgkmcnt(3)
	global_store_dwordx4 v150, v[168:171], s[6:7] nt
	s_waitcnt lgkmcnt(2)
	global_store_dwordx4 v150, v[172:175], s[6:7] offset:1024 nt
	s_waitcnt lgkmcnt(1)
	global_store_dwordx4 v150, v[176:179], s[6:7] offset:2048 nt
	s_waitcnt lgkmcnt(0)
	global_store_dwordx4 v150, v[180:183], s[6:7] offset:3072 nt
	s_add_u32 s6, s6, 0x8000
	s_addc_u32 s7, s7, 0
	s_waitcnt vmcnt(28)
	v_cvt_scalef32_pk_fp8_f32 v152, v184, v188, s5
	v_cvt_scalef32_pk_fp8_f32 v156, v185, v189, s5
	v_cvt_scalef32_pk_fp8_f32 v160, v186, v190, s5
	v_cvt_scalef32_pk_fp8_f32 v164, v187, v191, s5
	v_cvt_scalef32_pk_fp8_f32 v153, v200, v204, s5
	v_cvt_scalef32_pk_fp8_f32 v157, v201, v205, s5
	v_cvt_scalef32_pk_fp8_f32 v161, v202, v206, s5
	v_cvt_scalef32_pk_fp8_f32 v165, v203, v207, s5
	v_cvt_scalef32_pk_fp8_f32 v154, v216, v220, s5
	v_cvt_scalef32_pk_fp8_f32 v158, v217, v221, s5
	v_cvt_scalef32_pk_fp8_f32 v162, v218, v222, s5
	v_cvt_scalef32_pk_fp8_f32 v166, v219, v223, s5
	v_cvt_scalef32_pk_fp8_f32 v155, v232, v236, s5
	v_cvt_scalef32_pk_fp8_f32 v159, v233, v237, s5
	v_cvt_scalef32_pk_fp8_f32 v163, v234, v238, s5
	v_cvt_scalef32_pk_fp8_f32 v167, v235, v239, s5
	v_cvt_scalef32_pk_fp8_f32 v152, v192, v196, s5 op_sel:[0,0,0,1]
	v_cvt_scalef32_pk_fp8_f32 v156, v193, v197, s5 op_sel:[0,0,0,1]
	v_cvt_scalef32_pk_fp8_f32 v160, v194, v198, s5 op_sel:[0,0,0,1]
	v_cvt_scalef32_pk_fp8_f32 v164, v195, v199, s5 op_sel:[0,0,0,1]
	v_cvt_scalef32_pk_fp8_f32 v153, v208, v212, s5 op_sel:[0,0,0,1]
	v_cvt_scalef32_pk_fp8_f32 v157, v209, v213, s5 op_sel:[0,0,0,1]
	v_cvt_scalef32_pk_fp8_f32 v161, v210, v214, s5 op_sel:[0,0,0,1]
	v_cvt_scalef32_pk_fp8_f32 v165, v211, v215, s5 op_sel:[0,0,0,1]
	v_cvt_scalef32_pk_fp8_f32 v154, v224, v228, s5 op_sel:[0,0,0,1]
	v_cvt_scalef32_pk_fp8_f32 v158, v225, v229, s5 op_sel:[0,0,0,1]
	v_cvt_scalef32_pk_fp8_f32 v162, v226, v230, s5 op_sel:[0,0,0,1]
	v_cvt_scalef32_pk_fp8_f32 v166, v227, v231, s5 op_sel:[0,0,0,1]
	v_cvt_scalef32_pk_fp8_f32 v155, v240, v244, s5 op_sel:[0,0,0,1]
	v_cvt_scalef32_pk_fp8_f32 v159, v241, v245, s5 op_sel:[0,0,0,1]
	v_cvt_scalef32_pk_fp8_f32 v163, v242, v246, s5 op_sel:[0,0,0,1]
	v_cvt_scalef32_pk_fp8_f32 v167, v243, v247, s5 op_sel:[0,0,0,1]
	ds_write_b128 v148, v[152:155] offset:0
	ds_write_b128 v148, v[156:159] offset:128
	ds_write_b128 v149, v[160:163] offset:0
	ds_write_b128 v149, v[164:167] offset:128
	s_waitcnt lgkmcnt(0)
	s_barrier
	ds_read_b128 v[168:171], v150 offset:0
	ds_read_b128 v[172:175], v150 offset:1024
	ds_read_b128 v[176:179], v150 offset:2048
	ds_read_b128 v[180:183], v150 offset:3072
	s_waitcnt lgkmcnt(3)
	global_store_dwordx4 v150, v[168:171], s[6:7] nt
	s_waitcnt lgkmcnt(2)
	global_store_dwordx4 v150, v[172:175], s[6:7] offset:1024 nt
	s_waitcnt lgkmcnt(1)
	global_store_dwordx4 v150, v[176:179], s[6:7] offset:2048 nt
	s_waitcnt lgkmcnt(0)
	global_store_dwordx4 v150, v[180:183], s[6:7] offset:3072 nt
	s_add_u32 s6, s6, 0x8000
	s_addc_u32 s7, s7, 0
	s_waitcnt vmcnt(12)
	v_cvt_scalef32_pk_fp8_f32 v152, v0, v4, s5
	v_cvt_scalef32_pk_fp8_f32 v156, v1, v5, s5
	v_cvt_scalef32_pk_fp8_f32 v160, v2, v6, s5
	v_cvt_scalef32_pk_fp8_f32 v164, v3, v7, s5
	v_cvt_scalef32_pk_fp8_f32 v153, v16, v20, s5
	v_cvt_scalef32_pk_fp8_f32 v157, v17, v21, s5
	v_cvt_scalef32_pk_fp8_f32 v161, v18, v22, s5
	v_cvt_scalef32_pk_fp8_f32 v165, v19, v23, s5
	v_cvt_scalef32_pk_fp8_f32 v154, v32, v36, s5
	v_cvt_scalef32_pk_fp8_f32 v158, v33, v37, s5
	v_cvt_scalef32_pk_fp8_f32 v162, v34, v38, s5
	v_cvt_scalef32_pk_fp8_f32 v166, v35, v39, s5
	v_cvt_scalef32_pk_fp8_f32 v155, v48, v52, s5
	v_cvt_scalef32_pk_fp8_f32 v159, v49, v53, s5
	v_cvt_scalef32_pk_fp8_f32 v163, v50, v54, s5
	v_cvt_scalef32_pk_fp8_f32 v167, v51, v55, s5
	v_cvt_scalef32_pk_fp8_f32 v152, v8, v12, s5 op_sel:[0,0,0,1]
	v_cvt_scalef32_pk_fp8_f32 v156, v9, v13, s5 op_sel:[0,0,0,1]
	v_cvt_scalef32_pk_fp8_f32 v160, v10, v14, s5 op_sel:[0,0,0,1]
	v_cvt_scalef32_pk_fp8_f32 v164, v11, v15, s5 op_sel:[0,0,0,1]
	v_cvt_scalef32_pk_fp8_f32 v153, v24, v28, s5 op_sel:[0,0,0,1]
	v_cvt_scalef32_pk_fp8_f32 v157, v25, v29, s5 op_sel:[0,0,0,1]
	v_cvt_scalef32_pk_fp8_f32 v161, v26, v30, s5 op_sel:[0,0,0,1]
	v_cvt_scalef32_pk_fp8_f32 v165, v27, v31, s5 op_sel:[0,0,0,1]
	v_cvt_scalef32_pk_fp8_f32 v154, v40, v44, s5 op_sel:[0,0,0,1]
	v_cvt_scalef32_pk_fp8_f32 v158, v41, v45, s5 op_sel:[0,0,0,1]
	v_cvt_scalef32_pk_fp8_f32 v162, v42, v46, s5 op_sel:[0,0,0,1]
	v_cvt_scalef32_pk_fp8_f32 v166, v43, v47, s5 op_sel:[0,0,0,1]
	v_cvt_scalef32_pk_fp8_f32 v155, v56, v60, s5 op_sel:[0,0,0,1]
	v_cvt_scalef32_pk_fp8_f32 v159, v57, v61, s5 op_sel:[0,0,0,1]
	v_cvt_scalef32_pk_fp8_f32 v163, v58, v62, s5 op_sel:[0,0,0,1]
	v_cvt_scalef32_pk_fp8_f32 v167, v59, v63, s5 op_sel:[0,0,0,1]
	ds_write_b128 v148, v[152:155] offset:32768
	ds_write_b128 v148, v[156:159] offset:32896
	ds_write_b128 v149, v[160:163] offset:32768
	ds_write_b128 v149, v[164:167] offset:32896
	s_waitcnt lgkmcnt(0)
	s_barrier
	ds_read_b128 v[168:171], v150 offset:32768
	ds_read_b128 v[172:175], v150 offset:33792
	ds_read_b128 v[176:179], v150 offset:34816
	ds_read_b128 v[180:183], v150 offset:35840
	s_waitcnt lgkmcnt(3)
	global_store_dwordx4 v150, v[168:171], s[6:7] nt
	s_waitcnt lgkmcnt(2)
	global_store_dwordx4 v150, v[172:175], s[6:7] offset:1024 nt
	s_waitcnt lgkmcnt(1)
	global_store_dwordx4 v150, v[176:179], s[6:7] offset:2048 nt
	s_waitcnt lgkmcnt(0)
	global_store_dwordx4 v150, v[180:183], s[6:7] offset:3072 nt
	s_add_u32 s6, s6, 0x8000
	s_addc_u32 s7, s7, 0
	s_barrier
	s_cmp_lg_u32 vcc_hi, 0
	s_cbranch_scc1 .Lpc_skip
	v_mov_b32_e32 v152, 0
	v_mov_b32_e32 v153, 1
	v_cmp_eq_u32_e32 vcc, 0, v131
	s_and_saveexec_b64 s[4:5], vcc
	global_store_dword v152, v153, s[0:1] sc1
	s_mov_b64 exec, s[4:5]
